# v46 + code placement (9.3): 8 s_nop 0 pads ahead of load-segment waits so every MFMA cluster of the P2/P4/P5/P7/P8 K-loops starts at 0 mod 8 bytes
# speedup vs baseline: 1.0039x; 1.0005x over previous
; #define PG8_STAGE(bufoff, gbase, voff) do { _Pragma("unroll") for (int _i = 0; _i < 2; ++_i) \
;         __builtin_amdgcn_global_load_lds((const unsigned*)((const char*)(gbase) + (voff)[_i]), (LAS unsigned*)(lds + (bufoff) + ldsw + _i * 8192), 16, 0, 0); } while (0)
; #define PG8_LDA(dst, b, h) do { _Pragma("unroll") for (int m = 0; m < 4; ++m) { if constexpr (F8) dst##8[m] = PG8_LD32(lds + PG8_SA(b, h) + aoff + m * 2048); \
;         else { _Pragma("unroll") for (int k = 0; k < 2; ++k) dst[m][k] = *(const LAS bf16x8*)(lds + PG8_SA(b, h) + aoff + m * 2048 + k * 1024); } } } while (0)
; #define PG8_LDB(dst, b, h) do { _Pragma("unroll") for (int n = 0; n < 2; ++n) { if constexpr (F8) dst##8[n] = PG8_LD32(lds + PG8_SB(b, h) + boff + n * 2048); \
;         else { _Pragma("unroll") for (int k = 0; k < 2; ++k) dst[n][k] = *(const LAS bf16x8*)(lds + PG8_SB(b, h) + boff + n * 2048 + k * 1024); } } } while (0)
; #define PG8_WAIT_V(n) asm volatile("s_waitcnt vmcnt(" #n ")" ::: "memory")
; #define PG8_WAIT_L(n) asm volatile("s_waitcnt lgkmcnt(" #n ")" ::: "memory")
; #define PG8_BAR __builtin_amdgcn_s_barrier()
; #define PG8_SCHED __builtin_amdgcn_sched_barrier(0)
; template <class Epi, class Sched, bool GATHER, bool F8 = false>
; __device__ __forceinline__ void gemm_phase(LAS unsigned char* lds, const int K, const Sched& S, const Epi& E) {
;     ...
;         for (int t = 0; t < nt; t += 2) {
;             const bool last = (t == nt - 2);
;             const char* a1 = cA + (size_t)(t + 1) * kstep;
;             const char* a2 = last ? nA : cA + (size_t)(t + 2) * kstep; const char* b2 = last ? nB : cB + (size_t)(t + 2) * kstep;
;             const char* a3 = a2 + kstep; const char* b3 = b2 + kstep;
;             if constexpr (GATHER) { if (last && has_next) S.offsets(ui + 1, RA, CA, vN); }
;             PG8_LDB(B0, 0, 0); PG8_LDB(B1, 0, 1); PG8_SCHED; PG8_LDA(At, 0, 0); PG8_STAGE(PG8_SA(1, 1), a1, vA[1]);
;             PG8_WAIT_V(8); PG8_WAIT_L(0); PG8_BAR; PG8_MMA(0, 0, At, B0); PG8_MMA(0, 1, At, B1); PG8_BAR; PG8_SCHED;
;             PG8_LDA(At, 0, 1); PG8_STAGE(PG8_SB(0, 0), b2, voffB); PG8_STAGE(PG8_SB(0, 1), b2 + hstepB, voffB); PG8_STAGE(PG8_SA(0, 0), a2, vN[0]);
;             PG8_WAIT_V(8); PG8_WAIT_L(0); PG8_BAR; PG8_MMA(1, 0, At, B0); PG8_MMA(1, 1, At, B1); PG8_BAR; PG8_SCHED;
.LBB0_265:
	ds_read_b128 v[182:185], v177
	ds_read_b128 v[186:189], v177 offset:1024
	ds_read_b128 v[190:193], v177 offset:2048
	ds_read_b128 v[194:197], v177 offset:3072
	ds_read_b128 v[198:201], v178
	ds_read_b128 v[202:205], v178 offset:1024
	ds_read_b128 v[206:209], v178 offset:2048
	ds_read_b128 v[210:213], v178 offset:3072
	s_add_u32 s44, s0, 0x80
	s_addc_u32 s45, s1, 0
	s_cmp_eq_u32 vcc_lo, 28
	s_cselect_b32 s67, s49, s45
	s_cselect_b32 s66, s48, s44
	s_cselect_b32 s65, s63, s92
	s_cselect_b32 s64, s62, s12
	v_lshl_add_u64 v[246:247], s[0:1], 0, v[154:155]
	s_add_i32 m0, s72, 0xc000
	ds_read_b128 v[214:217], v179
	ds_read_b128 v[218:221], v179 offset:1024
	ds_read_b128 v[222:225], v179 offset:2048
	ds_read_b128 v[226:229], v179 offset:3072
	ds_read_b128 v[230:233], v179 offset:4096
	ds_read_b128 v[234:237], v179 offset:5120
	ds_read_b128 v[238:241], v179 offset:6144
	ds_read_b128 v[242:245], v179 offset:7168
	global_load_lds_dwordx4 v[246:247], off
	v_lshl_add_u64 v[246:247], s[0:1], 0, v[156:157]
	s_add_i32 m0, s72, 0xe000
	s_nop 0
	global_load_lds_dwordx4 v[246:247], off
	s_nop 0
	s_waitcnt vmcnt(8)
	s_waitcnt lgkmcnt(0)
	s_barrier
	s_setprio 1
	s_waitcnt lgkmcnt(0)
	v_mfma_f32_16x16x32_bf16 v[126:129], v[182:185], v[214:217], v[126:129]
	v_mfma_f32_16x16x32_bf16 v[122:125], v[190:193], v[214:217], v[122:125]
	v_mfma_f32_16x16x32_bf16 v[110:113], v[182:185], v[222:225], v[110:113]
	v_mfma_f32_16x16x32_bf16 v[106:109], v[190:193], v[222:225], v[106:109]
	v_mfma_f32_16x16x32_bf16 v[94:97], v[182:185], v[230:233], v[94:97]
	v_mfma_f32_16x16x32_bf16 v[90:93], v[190:193], v[230:233], v[90:93]
	v_mfma_f32_16x16x32_bf16 v[78:81], v[182:185], v[238:241], v[78:81]
	v_mfma_f32_16x16x32_bf16 v[74:77], v[190:193], v[238:241], v[74:77]
	v_mfma_f32_16x16x32_bf16 v[126:129], v[186:189], v[218:221], v[126:129]
	v_mfma_f32_16x16x32_bf16 v[122:125], v[194:197], v[218:221], v[122:125]
	v_mfma_f32_16x16x32_bf16 v[110:113], v[186:189], v[226:229], v[110:113]
	v_mfma_f32_16x16x32_bf16 v[106:109], v[194:197], v[226:229], v[106:109]
	v_mfma_f32_16x16x32_bf16 v[94:97], v[186:189], v[234:237], v[94:97]
	v_mfma_f32_16x16x32_bf16 v[90:93], v[194:197], v[234:237], v[90:93]
	v_mfma_f32_16x16x32_bf16 v[78:81], v[186:189], v[242:245], v[78:81]
	v_mfma_f32_16x16x32_bf16 v[74:77], v[194:197], v[242:245], v[74:77]
	s_setprio 0
	s_setprio 1
	v_mfma_f32_16x16x32_bf16 v[118:121], v[198:201], v[214:217], v[118:121]
	v_mfma_f32_16x16x32_bf16 v[114:117], v[206:209], v[214:217], v[114:117]
	v_mfma_f32_16x16x32_bf16 v[102:105], v[198:201], v[222:225], v[102:105]
	v_mfma_f32_16x16x32_bf16 v[98:101], v[206:209], v[222:225], v[98:101]
	v_mfma_f32_16x16x32_bf16 v[86:89], v[198:201], v[230:233], v[86:89]
	v_mfma_f32_16x16x32_bf16 v[82:85], v[206:209], v[230:233], v[82:85]
	v_mfma_f32_16x16x32_bf16 v[70:73], v[198:201], v[238:241], v[70:73]
	v_mfma_f32_16x16x32_bf16 v[66:69], v[206:209], v[238:241], v[66:69]
	v_mfma_f32_16x16x32_bf16 v[118:121], v[202:205], v[218:221], v[118:121]
	v_mfma_f32_16x16x32_bf16 v[114:117], v[210:213], v[218:221], v[114:117]
	v_mfma_f32_16x16x32_bf16 v[102:105], v[202:205], v[226:229], v[102:105]
	v_mfma_f32_16x16x32_bf16 v[98:101], v[210:213], v[226:229], v[98:101]
	v_mfma_f32_16x16x32_bf16 v[86:89], v[202:205], v[234:237], v[86:89]
	v_mfma_f32_16x16x32_bf16 v[82:85], v[210:213], v[234:237], v[82:85]
	v_mfma_f32_16x16x32_bf16 v[70:73], v[202:205], v[242:245], v[70:73]
	v_mfma_f32_16x16x32_bf16 v[66:69], v[210:213], v[242:245], v[66:69]
	s_setprio 0
	s_barrier
	s_add_i32 s44, s90, s71
	v_lshl_add_u64 v[246:247], s[64:65], 0, v[130:131]
	s_mov_b32 m0, s44
	ds_read_b128 v[214:217], v179 offset:16384
	ds_read_b128 v[218:221], v179 offset:17408
	ds_read_b128 v[222:225], v179 offset:18432
	ds_read_b128 v[226:229], v179 offset:19456
	ds_read_b128 v[230:233], v179 offset:20480
	ds_read_b128 v[234:237], v179 offset:21504
	ds_read_b128 v[238:241], v179 offset:22528
	ds_read_b128 v[242:245], v179 offset:23552
	global_load_lds_dwordx4 v[246:247], off
	s_add_i32 m0, s44, 0x2000
	s_add_u32 s84, s64, 0x20000
	v_lshl_add_u64 v[248:249], s[64:65], 0, v[136:137]
	s_addc_u32 s85, s65, 0
	s_add_i32 s44, s91, s71
	global_load_lds_dwordx4 v[248:249], off
	v_lshl_add_u64 v[250:251], s[84:85], 0, v[130:131]
	s_mov_b32 m0, s44
	v_lshl_add_u64 v[252:253], s[66:67], 0, v[138:139]
	global_load_lds_dwordx4 v[250:251], off
	v_lshl_add_u64 v[250:251], s[84:85], 0, v[136:137]
	s_add_i32 m0, s44, 0x2000
	s_nop 0
	global_load_lds_dwordx4 v[250:251], off
	v_lshl_add_u64 v[250:251], s[66:67], 0, v[132:133]
	s_mov_b32 m0, s72
	s_nop 0
	global_load_lds_dwordx4 v[250:251], off
	s_mov_b32 m0, s73
	s_nop 0
	global_load_lds_dwordx4 v[252:253], off
	s_nop 0
	s_waitcnt vmcnt(8)
	s_waitcnt lgkmcnt(0)
	s_barrier
; #define PG8_STAGE(bufoff, gbase, voff) do { _Pragma("unroll") for (int _i = 0; _i < 2; ++_i) \
;         __builtin_amdgcn_global_load_lds((const unsigned*)((const char*)(gbase) + (voff)[_i]), (LAS unsigned*)(lds + (bufoff) + ldsw + _i * 8192), 16, 0, 0); } while (0)
; #define PG8_LDA(dst, b, h) do { _Pragma("unroll") for (int m = 0; m < 4; ++m) { if constexpr (F8) dst##8[m] = PG8_LD32(lds + PG8_SA(b, h) + aoff + m * 2048); \
;         else { _Pragma("unroll") for (int k = 0; k < 2; ++k) dst[m][k] = *(const LAS bf16x8*)(lds + PG8_SA(b, h) + aoff + m * 2048 + k * 1024); } } } while (0)
; #define PG8_LDB(dst, b, h) do { _Pragma("unroll") for (int n = 0; n < 2; ++n) { if constexpr (F8) dst##8[n] = PG8_LD32(lds + PG8_SB(b, h) + boff + n * 2048); \
;         else { _Pragma("unroll") for (int k = 0; k < 2; ++k) dst[n][k] = *(const LAS bf16x8*)(lds + PG8_SB(b, h) + boff + n * 2048 + k * 1024); } } } while (0)
; #define PG8_WAIT_V(n) asm volatile("s_waitcnt vmcnt(" #n ")" ::: "memory")
; #define PG8_WAIT_L(n) asm volatile("s_waitcnt lgkmcnt(" #n ")" ::: "memory")
; #define PG8_BAR __builtin_amdgcn_s_barrier()
; #define PG8_SCHED __builtin_amdgcn_sched_barrier(0)
; template <class Epi, class Sched, bool GATHER, bool F8 = false>
; __device__ __forceinline__ void gemm_phase(LAS unsigned char* lds, const int K, const Sched& S, const Epi& E) {
;     ...
;             PG8_WAIT_V(8); PG8_WAIT_L(0); PG8_BAR; PG8_MMA(1, 0, At, B0); PG8_MMA(1, 1, At, B1); PG8_BAR; PG8_SCHED;
;             PG8_LDB(B0, 1, 0); PG8_LDB(B1, 1, 1); PG8_SCHED; PG8_LDA(At, 1, 0); PG8_STAGE(PG8_SA(0, 1), a2, vN[1]);
;             PG8_WAIT_V(8); PG8_WAIT_L(0); PG8_BAR; PG8_MMA(0, 0, At, B0); PG8_MMA(0, 1, At, B1); PG8_BAR; PG8_SCHED;
	s_setprio 1
	s_waitcnt lgkmcnt(0)
	v_mfma_f32_16x16x32_bf16 v[62:65], v[182:185], v[214:217], v[62:65]
	v_mfma_f32_16x16x32_bf16 v[58:61], v[190:193], v[214:217], v[58:61]
	v_mfma_f32_16x16x32_bf16 v[46:49], v[182:185], v[222:225], v[46:49]
	v_mfma_f32_16x16x32_bf16 v[42:45], v[190:193], v[222:225], v[42:45]
	v_mfma_f32_16x16x32_bf16 v[30:33], v[182:185], v[230:233], v[30:33]
	v_mfma_f32_16x16x32_bf16 v[26:29], v[190:193], v[230:233], v[26:29]
	v_mfma_f32_16x16x32_bf16 v[14:17], v[182:185], v[238:241], v[14:17]
	v_mfma_f32_16x16x32_bf16 v[10:13], v[190:193], v[238:241], v[10:13]
	v_mfma_f32_16x16x32_bf16 v[62:65], v[186:189], v[218:221], v[62:65]
	v_mfma_f32_16x16x32_bf16 v[58:61], v[194:197], v[218:221], v[58:61]
	v_mfma_f32_16x16x32_bf16 v[46:49], v[186:189], v[226:229], v[46:49]
	v_mfma_f32_16x16x32_bf16 v[42:45], v[194:197], v[226:229], v[42:45]
	v_mfma_f32_16x16x32_bf16 v[30:33], v[186:189], v[234:237], v[30:33]
	v_mfma_f32_16x16x32_bf16 v[26:29], v[194:197], v[234:237], v[26:29]
	v_mfma_f32_16x16x32_bf16 v[14:17], v[186:189], v[242:245], v[14:17]
	v_mfma_f32_16x16x32_bf16 v[10:13], v[194:197], v[242:245], v[10:13]
	s_setprio 0
	s_setprio 1
	v_mfma_f32_16x16x32_bf16 v[54:57], v[198:201], v[214:217], v[54:57]
	v_mfma_f32_16x16x32_bf16 v[50:53], v[206:209], v[214:217], v[50:53]
	v_mfma_f32_16x16x32_bf16 v[38:41], v[198:201], v[222:225], v[38:41]
	v_mfma_f32_16x16x32_bf16 v[34:37], v[206:209], v[222:225], v[34:37]
	v_mfma_f32_16x16x32_bf16 v[22:25], v[198:201], v[230:233], v[22:25]
	v_mfma_f32_16x16x32_bf16 v[18:21], v[206:209], v[230:233], v[18:21]
	v_mfma_f32_16x16x32_bf16 v[6:9], v[198:201], v[238:241], v[6:9]
	v_mfma_f32_16x16x32_bf16 v[2:5], v[206:209], v[238:241], v[2:5]
	v_mfma_f32_16x16x32_bf16 v[54:57], v[202:205], v[218:221], v[54:57]
	v_mfma_f32_16x16x32_bf16 v[50:53], v[210:213], v[218:221], v[50:53]
	v_mfma_f32_16x16x32_bf16 v[38:41], v[202:205], v[226:229], v[38:41]
	v_mfma_f32_16x16x32_bf16 v[34:37], v[210:213], v[226:229], v[34:37]
	v_mfma_f32_16x16x32_bf16 v[22:25], v[202:205], v[234:237], v[22:25]
	v_mfma_f32_16x16x32_bf16 v[18:21], v[210:213], v[234:237], v[18:21]
	v_mfma_f32_16x16x32_bf16 v[6:9], v[202:205], v[242:245], v[6:9]
	v_mfma_f32_16x16x32_bf16 v[2:5], v[210:213], v[242:245], v[2:5]
	s_setprio 0
	s_barrier
	s_add_i32 s44, 0, 0x18000
	v_add_u32_e32 v142, s44, v166
	s_add_i32 s45, 0, 0x1c000
	ds_read_b128 v[182:185], v142
	ds_read_b128 v[186:189], v142 offset:1024
	ds_read_b128 v[190:193], v142 offset:2048
	ds_read_b128 v[194:197], v142 offset:3072
	v_add_u32_e32 v142, s45, v166
	ds_read_b128 v[198:201], v142
	ds_read_b128 v[202:205], v142 offset:1024
	ds_read_b128 v[206:209], v142 offset:2048
	ds_read_b128 v[210:213], v142 offset:3072
	s_mov_b32 m0, s74
	v_lshl_add_u64 v[158:159], s[66:67], 0, v[134:135]
	ds_read_b128 v[214:217], v179 offset:32768
	ds_read_b128 v[218:221], v179 offset:33792
	ds_read_b128 v[222:225], v179 offset:34816
	ds_read_b128 v[226:229], v179 offset:35840
	ds_read_b128 v[230:233], v179 offset:36864
	ds_read_b128 v[234:237], v179 offset:37888
	ds_read_b128 v[238:241], v179 offset:38912
	ds_read_b128 v[242:245], v179 offset:39936
	global_load_lds_dwordx4 v[158:159], off
	v_lshl_add_u64 v[158:159], s[66:67], 0, v[140:141]
	s_mov_b32 m0, s75
	s_nop 0
	global_load_lds_dwordx4 v[158:159], off
	s_waitcnt vmcnt(8)
	s_waitcnt lgkmcnt(0)
	s_barrier
	s_setprio 1
	s_waitcnt lgkmcnt(0)
	v_mfma_f32_16x16x32_bf16 v[126:129], v[182:185], v[214:217], v[126:129]
	v_mfma_f32_16x16x32_bf16 v[122:125], v[190:193], v[214:217], v[122:125]
	v_mfma_f32_16x16x32_bf16 v[110:113], v[182:185], v[222:225], v[110:113]
	v_mfma_f32_16x16x32_bf16 v[106:109], v[190:193], v[222:225], v[106:109]
	v_mfma_f32_16x16x32_bf16 v[94:97], v[182:185], v[230:233], v[94:97]
	v_mfma_f32_16x16x32_bf16 v[90:93], v[190:193], v[230:233], v[90:93]
	v_mfma_f32_16x16x32_bf16 v[78:81], v[182:185], v[238:241], v[78:81]
	v_mfma_f32_16x16x32_bf16 v[74:77], v[190:193], v[238:241], v[74:77]
	v_mfma_f32_16x16x32_bf16 v[126:129], v[186:189], v[218:221], v[126:129]
	v_mfma_f32_16x16x32_bf16 v[122:125], v[194:197], v[218:221], v[122:125]
	v_mfma_f32_16x16x32_bf16 v[110:113], v[186:189], v[226:229], v[110:113]
	v_mfma_f32_16x16x32_bf16 v[106:109], v[194:197], v[226:229], v[106:109]
	v_mfma_f32_16x16x32_bf16 v[94:97], v[186:189], v[234:237], v[94:97]
	v_mfma_f32_16x16x32_bf16 v[90:93], v[194:197], v[234:237], v[90:93]
	v_mfma_f32_16x16x32_bf16 v[78:81], v[186:189], v[242:245], v[78:81]
	v_mfma_f32_16x16x32_bf16 v[74:77], v[194:197], v[242:245], v[74:77]
	s_setprio 0
	s_setprio 1
	v_mfma_f32_16x16x32_bf16 v[118:121], v[198:201], v[214:217], v[118:121]
	v_mfma_f32_16x16x32_bf16 v[114:117], v[206:209], v[214:217], v[114:117]
	v_mfma_f32_16x16x32_bf16 v[102:105], v[198:201], v[222:225], v[102:105]
	v_mfma_f32_16x16x32_bf16 v[98:101], v[206:209], v[222:225], v[98:101]
	v_mfma_f32_16x16x32_bf16 v[86:89], v[198:201], v[230:233], v[86:89]
	v_mfma_f32_16x16x32_bf16 v[82:85], v[206:209], v[230:233], v[82:85]
	v_mfma_f32_16x16x32_bf16 v[70:73], v[198:201], v[238:241], v[70:73]
	v_mfma_f32_16x16x32_bf16 v[66:69], v[206:209], v[238:241], v[66:69]
	v_mfma_f32_16x16x32_bf16 v[118:121], v[202:205], v[218:221], v[118:121]
	v_mfma_f32_16x16x32_bf16 v[114:117], v[210:213], v[218:221], v[114:117]
	v_mfma_f32_16x16x32_bf16 v[102:105], v[202:205], v[226:229], v[102:105]
	v_mfma_f32_16x16x32_bf16 v[98:101], v[210:213], v[226:229], v[98:101]
	v_mfma_f32_16x16x32_bf16 v[86:89], v[202:205], v[234:237], v[86:89]
	v_mfma_f32_16x16x32_bf16 v[82:85], v[210:213], v[234:237], v[82:85]
	v_mfma_f32_16x16x32_bf16 v[70:73], v[202:205], v[242:245], v[70:73]
	v_mfma_f32_16x16x32_bf16 v[66:69], v[210:213], v[242:245], v[66:69]
	s_setprio 0
	s_barrier
; #define PG8_STAGE(bufoff, gbase, voff) do { _Pragma("unroll") for (int _i = 0; _i < 2; ++_i) \
;         __builtin_amdgcn_global_load_lds((const unsigned*)((const char*)(gbase) + (voff)[_i]), (LAS unsigned*)(lds + (bufoff) + ldsw + _i * 8192), 16, 0, 0); } while (0)
; #define PG8_LDA(dst, b, h) do { _Pragma("unroll") for (int m = 0; m < 4; ++m) { if constexpr (F8) dst##8[m] = PG8_LD32(lds + PG8_SA(b, h) + aoff + m * 2048); \
;         else { _Pragma("unroll") for (int k = 0; k < 2; ++k) dst[m][k] = *(const LAS bf16x8*)(lds + PG8_SA(b, h) + aoff + m * 2048 + k * 1024); } } } while (0)
; #define PG8_WAIT_V(n) asm volatile("s_waitcnt vmcnt(" #n ")" ::: "memory")
; #define PG8_WAIT_L(n) asm volatile("s_waitcnt lgkmcnt(" #n ")" ::: "memory")
; #define PG8_BAR __builtin_amdgcn_s_barrier()
; #define PG8_SCHED __builtin_amdgcn_sched_barrier(0)
; template <class Epi, class Sched, bool GATHER, bool F8 = false>
; __device__ __forceinline__ void gemm_phase(LAS unsigned char* lds, const int K, const Sched& S, const Epi& E) {
;     ...
;             PG8_LDA(At, 1, 1); PG8_STAGE(PG8_SB(1, 0), b3, voffB); PG8_STAGE(PG8_SB(1, 1), b3 + hstepB, voffB); PG8_STAGE(PG8_SA(1, 0), a3, vN[0]);
;             PG8_WAIT_V(8); PG8_WAIT_L(0); PG8_BAR; PG8_MMA(1, 0, At, B0); PG8_MMA(1, 1, At, B1); PG8_BAR; PG8_SCHED;
;         }
;         if (wr == 0) PG8_BAR;
	s_add_i32 s44, s44, s71
	v_lshl_add_u64 v[158:159], v[246:247], 0, s[20:21]
	s_mov_b32 m0, s44
	ds_read_b128 v[214:217], v179 offset:49152
	ds_read_b128 v[218:221], v179 offset:50176
	ds_read_b128 v[222:225], v179 offset:51200
	ds_read_b128 v[226:229], v179 offset:52224
	ds_read_b128 v[230:233], v179 offset:53248
	ds_read_b128 v[234:237], v179 offset:54272
	ds_read_b128 v[238:241], v179 offset:55296
	ds_read_b128 v[242:245], v179 offset:56320
	global_load_lds_dwordx4 v[158:159], off
	s_add_i32 m0, s44, 0x2000
	s_add_u32 s64, s64, 0x20080
	v_lshl_add_u64 v[158:159], v[248:249], 0, s[20:21]
	s_addc_u32 s65, s65, 0
	s_add_i32 s44, s45, s71
	global_load_lds_dwordx4 v[158:159], off
	v_lshl_add_u64 v[158:159], s[64:65], 0, v[130:131]
	s_mov_b32 m0, s44
	s_nop 0
	global_load_lds_dwordx4 v[158:159], off
	v_lshl_add_u64 v[158:159], s[64:65], 0, v[136:137]
	s_add_i32 m0, s44, 0x2000
	s_nop 0
	global_load_lds_dwordx4 v[158:159], off
	v_lshl_add_u64 v[158:159], v[250:251], 0, s[20:21]
	s_mov_b32 m0, s77
	s_nop 0
	global_load_lds_dwordx4 v[158:159], off
	v_lshl_add_u64 v[158:159], v[252:253], 0, s[20:21]
	s_mov_b32 m0, s78
	s_nop 0
	global_load_lds_dwordx4 v[158:159], off
	s_waitcnt vmcnt(8)
	s_waitcnt lgkmcnt(0)
	s_barrier
	s_setprio 1
	s_waitcnt lgkmcnt(0)
	v_mfma_f32_16x16x32_bf16 v[62:65], v[182:185], v[214:217], v[62:65]
	v_mfma_f32_16x16x32_bf16 v[58:61], v[190:193], v[214:217], v[58:61]
	v_mfma_f32_16x16x32_bf16 v[46:49], v[182:185], v[222:225], v[46:49]
	v_mfma_f32_16x16x32_bf16 v[42:45], v[190:193], v[222:225], v[42:45]
	v_mfma_f32_16x16x32_bf16 v[30:33], v[182:185], v[230:233], v[30:33]
	v_mfma_f32_16x16x32_bf16 v[26:29], v[190:193], v[230:233], v[26:29]
	v_mfma_f32_16x16x32_bf16 v[14:17], v[182:185], v[238:241], v[14:17]
	v_mfma_f32_16x16x32_bf16 v[10:13], v[190:193], v[238:241], v[10:13]
	v_mfma_f32_16x16x32_bf16 v[62:65], v[186:189], v[218:221], v[62:65]
	v_mfma_f32_16x16x32_bf16 v[58:61], v[194:197], v[218:221], v[58:61]
	v_mfma_f32_16x16x32_bf16 v[46:49], v[186:189], v[226:229], v[46:49]
	v_mfma_f32_16x16x32_bf16 v[42:45], v[194:197], v[226:229], v[42:45]
	v_mfma_f32_16x16x32_bf16 v[30:33], v[186:189], v[234:237], v[30:33]
	v_mfma_f32_16x16x32_bf16 v[26:29], v[194:197], v[234:237], v[26:29]
	v_mfma_f32_16x16x32_bf16 v[14:17], v[186:189], v[242:245], v[14:17]
	v_mfma_f32_16x16x32_bf16 v[10:13], v[194:197], v[242:245], v[10:13]
	s_setprio 0
	s_setprio 1
	v_mfma_f32_16x16x32_bf16 v[54:57], v[198:201], v[214:217], v[54:57]
	v_mfma_f32_16x16x32_bf16 v[50:53], v[206:209], v[214:217], v[50:53]
	v_mfma_f32_16x16x32_bf16 v[38:41], v[198:201], v[222:225], v[38:41]
	v_mfma_f32_16x16x32_bf16 v[34:37], v[206:209], v[222:225], v[34:37]
	v_mfma_f32_16x16x32_bf16 v[22:25], v[198:201], v[230:233], v[22:25]
	v_mfma_f32_16x16x32_bf16 v[18:21], v[206:209], v[230:233], v[18:21]
	v_mfma_f32_16x16x32_bf16 v[6:9], v[198:201], v[238:241], v[6:9]
	v_mfma_f32_16x16x32_bf16 v[2:5], v[206:209], v[238:241], v[2:5]
	v_mfma_f32_16x16x32_bf16 v[54:57], v[202:205], v[218:221], v[54:57]
	v_mfma_f32_16x16x32_bf16 v[50:53], v[210:213], v[218:221], v[50:53]
	v_mfma_f32_16x16x32_bf16 v[38:41], v[202:205], v[226:229], v[38:41]
	v_mfma_f32_16x16x32_bf16 v[34:37], v[210:213], v[226:229], v[34:37]
	v_mfma_f32_16x16x32_bf16 v[22:25], v[202:205], v[234:237], v[22:25]
	v_mfma_f32_16x16x32_bf16 v[18:21], v[210:213], v[234:237], v[18:21]
	v_mfma_f32_16x16x32_bf16 v[6:9], v[202:205], v[242:245], v[6:9]
	v_mfma_f32_16x16x32_bf16 v[2:5], v[210:213], v[242:245], v[2:5]
	s_setprio 0
	s_barrier
	s_add_i32 vcc_lo, vcc_lo, 2
	s_add_u32 s0, s0, 0x100
	s_addc_u32 s1, s1, 0
	s_add_u32 s12, s12, 0x100
	s_addc_u32 s92, s92, 0
	s_cmp_gt_u32 vcc_lo, 29
	s_cbranch_scc0 .LBB0_265
	s_and_b64 vcc, exec, s[24:25]
	s_cbranch_vccz .LBB0_268
	s_barrier

; #define PG8_STAGE(bufoff, gbase, voff) do { _Pragma("unroll") for (int _i = 0; _i < 2; ++_i) \
;         __builtin_amdgcn_global_load_lds((const unsigned*)((const char*)(gbase) + (voff)[_i]), (LAS unsigned*)(lds + (bufoff) + ldsw + _i * 8192), 16, 0, 0); } while (0)
; #define PG8_LDA(dst, b, h) do { _Pragma("unroll") for (int m = 0; m < 4; ++m) { if constexpr (F8) dst##8[m] = PG8_LD32(lds + PG8_SA(b, h) + aoff + m * 2048); \
;         else { _Pragma("unroll") for (int k = 0; k < 2; ++k) dst[m][k] = *(const LAS bf16x8*)(lds + PG8_SA(b, h) + aoff + m * 2048 + k * 1024); } } } while (0)
; #define PG8_LDB(dst, b, h) do { _Pragma("unroll") for (int n = 0; n < 2; ++n) { if constexpr (F8) dst##8[n] = PG8_LD32(lds + PG8_SB(b, h) + boff + n * 2048); \
;         else { _Pragma("unroll") for (int k = 0; k < 2; ++k) dst[n][k] = *(const LAS bf16x8*)(lds + PG8_SB(b, h) + boff + n * 2048 + k * 1024); } } } while (0)
; #define PG8_WAIT_V(n) asm volatile("s_waitcnt vmcnt(" #n ")" ::: "memory")
; #define PG8_WAIT_L(n) asm volatile("s_waitcnt lgkmcnt(" #n ")" ::: "memory")
; #define PG8_BAR __builtin_amdgcn_s_barrier()
; #define PG8_SCHED __builtin_amdgcn_sched_barrier(0)
; template <class Epi, class Sched, bool GATHER, bool F8 = false>
; __device__ __forceinline__ void gemm_phase(LAS unsigned char* lds, const int K, const Sched& S, const Epi& E) {
;     ...
;             PG8_LDB(B0, 0, 0); PG8_LDB(B1, 0, 1); PG8_SCHED; PG8_LDA(At, 0, 0); PG8_STAGE(PG8_SA(1, 1), a1, vA[1]);
;             PG8_WAIT_V(8); PG8_WAIT_L(0); PG8_BAR; PG8_MMA(0, 0, At, B0); PG8_MMA(0, 1, At, B1); PG8_BAR; PG8_SCHED;
;             PG8_LDA(At, 0, 1); PG8_STAGE(PG8_SB(0, 0), b2, voffB); PG8_STAGE(PG8_SB(0, 1), b2 + hstepB, voffB); PG8_STAGE(PG8_SA(0, 0), a2, vN[0]);
;             PG8_WAIT_V(8); PG8_WAIT_L(0); PG8_BAR; PG8_MMA(1, 0, At, B0); PG8_MMA(1, 1, At, B1); PG8_BAR; PG8_SCHED;
.LBB0_346:
	ds_read_b128 v[18:21], v1
	ds_read_b128 v[22:25], v1 offset:1024
	ds_read_b128 v[26:29], v1 offset:2048
	ds_read_b128 v[30:33], v1 offset:3072
	ds_read_b128 v[2:5], v207
	ds_read_b128 v[6:9], v207 offset:1024
	ds_read_b128 v[10:13], v207 offset:2048
	ds_read_b128 v[14:17], v207 offset:3072
	s_add_u32 s48, s46, 0x80
	s_addc_u32 s49, s47, 0
	s_cmp_eq_u32 s97, 12
	s_cselect_b32 s63, s86, s49
	s_cselect_b32 s62, s87, s48
	s_cselect_b32 s49, s91, s96
	s_cselect_b32 s48, s92, s95
	v_lshl_add_u64 v[236:237], s[46:47], 0, v[178:179]
	s_add_i32 m0, s66, 0xc000
	ds_read_b128 v[182:185], v208
	ds_read_b128 v[186:189], v208 offset:1024
	ds_read_b128 v[212:215], v208 offset:2048
	ds_read_b128 v[216:219], v208 offset:3072
	ds_read_b128 v[220:223], v208 offset:4096
	ds_read_b128 v[224:227], v208 offset:5120
	ds_read_b128 v[228:231], v208 offset:6144
	ds_read_b128 v[232:235], v208 offset:7168
	global_load_lds_dwordx4 v[236:237], off
	v_lshl_add_u64 v[236:237], s[46:47], 0, v[180:181]
	s_add_i32 m0, s66, 0xe000
	s_nop 0
	global_load_lds_dwordx4 v[236:237], off
	s_nop 0
	s_waitcnt vmcnt(8)
	s_waitcnt lgkmcnt(0)
	s_barrier
	s_setprio 1
	s_waitcnt lgkmcnt(0)
	v_mfma_scale_f32_16x16x128_f8f6f4 v[158:161], v[18:25], v[182:189], v[158:161], v190, v190 op_sel_hi:[0,0,0]
	v_mfma_scale_f32_16x16x128_f8f6f4 v[154:157], v[26:33], v[182:189], v[154:157], v190, v190 op_sel_hi:[0,0,0]
	v_mfma_scale_f32_16x16x128_f8f6f4 v[142:145], v[18:25], v[212:219], v[142:145], v190, v190 op_sel_hi:[0,0,0]
	v_mfma_scale_f32_16x16x128_f8f6f4 v[138:141], v[26:33], v[212:219], v[138:141], v190, v190 op_sel_hi:[0,0,0]
	v_mfma_scale_f32_16x16x128_f8f6f4 v[126:129], v[18:25], v[220:227], v[126:129], v190, v190 op_sel_hi:[0,0,0]
	v_mfma_scale_f32_16x16x128_f8f6f4 v[122:125], v[26:33], v[220:227], v[122:125], v190, v190 op_sel_hi:[0,0,0]
	v_mfma_scale_f32_16x16x128_f8f6f4 v[110:113], v[18:25], v[228:235], v[110:113], v190, v190 op_sel_hi:[0,0,0]
	v_mfma_scale_f32_16x16x128_f8f6f4 v[106:109], v[26:33], v[228:235], v[106:109], v190, v190 op_sel_hi:[0,0,0]
	s_setprio 0
	s_setprio 1
	v_mfma_scale_f32_16x16x128_f8f6f4 v[150:153], v[2:9], v[182:189], v[150:153], v190, v190 op_sel_hi:[0,0,0]
	v_mfma_scale_f32_16x16x128_f8f6f4 v[146:149], v[10:17], v[182:189], v[146:149], v190, v190 op_sel_hi:[0,0,0]
	v_mfma_scale_f32_16x16x128_f8f6f4 v[134:137], v[2:9], v[212:219], v[134:137], v190, v190 op_sel_hi:[0,0,0]
	v_mfma_scale_f32_16x16x128_f8f6f4 v[130:133], v[10:17], v[212:219], v[130:133], v190, v190 op_sel_hi:[0,0,0]
	v_mfma_scale_f32_16x16x128_f8f6f4 v[118:121], v[2:9], v[220:227], v[118:121], v190, v190 op_sel_hi:[0,0,0]
	v_mfma_scale_f32_16x16x128_f8f6f4 v[114:117], v[10:17], v[220:227], v[114:117], v190, v190 op_sel_hi:[0,0,0]
	v_mfma_scale_f32_16x16x128_f8f6f4 v[102:105], v[2:9], v[228:235], v[102:105], v190, v190 op_sel_hi:[0,0,0]
	v_mfma_scale_f32_16x16x128_f8f6f4 v[98:101], v[10:17], v[228:235], v[98:101], v190, v190 op_sel_hi:[0,0,0]
	s_setprio 0
	s_barrier
	s_add_i32 s84, s77, s65
	v_lshl_add_u64 v[182:183], s[48:49], 0, v[162:163]
	s_mov_b32 m0, s84
	ds_read_b128 v[212:215], v208 offset:16384
	ds_read_b128 v[216:219], v208 offset:17408
	ds_read_b128 v[220:223], v208 offset:18432
	ds_read_b128 v[224:227], v208 offset:19456
	ds_read_b128 v[228:231], v208 offset:20480
	ds_read_b128 v[232:235], v208 offset:21504
	ds_read_b128 v[236:239], v208 offset:22528
	ds_read_b128 v[240:243], v208 offset:23552
	global_load_lds_dwordx4 v[182:183], off
	s_add_i32 m0, s84, 0x2000
	s_add_u32 s84, s48, 0x10000
	v_lshl_add_u64 v[184:185], s[48:49], 0, v[168:169]
	s_addc_u32 s85, s49, 0
	s_add_i32 s93, s78, s65
	global_load_lds_dwordx4 v[184:185], off
	v_lshl_add_u64 v[186:187], s[84:85], 0, v[162:163]
	s_mov_b32 m0, s93
	v_lshl_add_u64 v[188:189], s[62:63], 0, v[172:173]
	global_load_lds_dwordx4 v[186:187], off
	v_lshl_add_u64 v[186:187], s[84:85], 0, v[168:169]
	s_add_i32 m0, s93, 0x2000
	s_nop 0
	global_load_lds_dwordx4 v[186:187], off
	v_lshl_add_u64 v[186:187], s[62:63], 0, v[164:165]
	s_mov_b32 m0, s66
	s_nop 0
	global_load_lds_dwordx4 v[186:187], off
	s_mov_b32 m0, s67
	s_nop 0
	global_load_lds_dwordx4 v[188:189], off
	s_nop 0
	s_waitcnt vmcnt(8)
	s_waitcnt lgkmcnt(0)
	s_barrier
	s_setprio 1
	s_waitcnt lgkmcnt(0)
	v_mfma_scale_f32_16x16x128_f8f6f4 v[94:97], v[18:25], v[212:219], v[94:97], v190, v190 op_sel_hi:[0,0,0]
	v_mfma_scale_f32_16x16x128_f8f6f4 v[90:93], v[26:33], v[212:219], v[90:93], v190, v190 op_sel_hi:[0,0,0]
	v_mfma_scale_f32_16x16x128_f8f6f4 v[78:81], v[18:25], v[220:227], v[78:81], v190, v190 op_sel_hi:[0,0,0]
	v_mfma_scale_f32_16x16x128_f8f6f4 v[74:77], v[26:33], v[220:227], v[74:77], v190, v190 op_sel_hi:[0,0,0]
	v_mfma_scale_f32_16x16x128_f8f6f4 v[62:65], v[18:25], v[228:235], v[62:65], v190, v190 op_sel_hi:[0,0,0]
	v_mfma_scale_f32_16x16x128_f8f6f4 v[58:61], v[26:33], v[228:235], v[58:61], v190, v190 op_sel_hi:[0,0,0]
	v_mfma_scale_f32_16x16x128_f8f6f4 v[46:49], v[18:25], v[236:243], v[46:49], v190, v190 op_sel_hi:[0,0,0]
	v_mfma_scale_f32_16x16x128_f8f6f4 v[42:45], v[26:33], v[236:243], v[42:45], v190, v190 op_sel_hi:[0,0,0]
	s_setprio 0
	s_setprio 1
	v_mfma_scale_f32_16x16x128_f8f6f4 v[86:89], v[2:9], v[212:219], v[86:89], v190, v190 op_sel_hi:[0,0,0]
	v_mfma_scale_f32_16x16x128_f8f6f4 v[82:85], v[10:17], v[212:219], v[82:85], v190, v190 op_sel_hi:[0,0,0]
	v_mfma_scale_f32_16x16x128_f8f6f4 v[70:73], v[2:9], v[220:227], v[70:73], v190, v190 op_sel_hi:[0,0,0]
	v_mfma_scale_f32_16x16x128_f8f6f4 v[66:69], v[10:17], v[220:227], v[66:69], v190, v190 op_sel_hi:[0,0,0]
	v_mfma_scale_f32_16x16x128_f8f6f4 v[54:57], v[2:9], v[228:235], v[54:57], v190, v190 op_sel_hi:[0,0,0]
	v_mfma_scale_f32_16x16x128_f8f6f4 v[50:53], v[10:17], v[228:235], v[50:53], v190, v190 op_sel_hi:[0,0,0]
	v_mfma_scale_f32_16x16x128_f8f6f4 v[38:41], v[2:9], v[236:243], v[38:41], v190, v190 op_sel_hi:[0,0,0]
	v_mfma_scale_f32_16x16x128_f8f6f4 v[34:37], v[10:17], v[236:243], v[34:37], v190, v190 op_sel_hi:[0,0,0]
	s_setprio 0
	s_barrier
; #define PG8_STAGE(bufoff, gbase, voff) do { _Pragma("unroll") for (int _i = 0; _i < 2; ++_i) \
;         __builtin_amdgcn_global_load_lds((const unsigned*)((const char*)(gbase) + (voff)[_i]), (LAS unsigned*)(lds + (bufoff) + ldsw + _i * 8192), 16, 0, 0); } while (0)
; #define PG8_LDA(dst, b, h) do { _Pragma("unroll") for (int m = 0; m < 4; ++m) { if constexpr (F8) dst##8[m] = PG8_LD32(lds + PG8_SA(b, h) + aoff + m * 2048); \
;         else { _Pragma("unroll") for (int k = 0; k < 2; ++k) dst[m][k] = *(const LAS bf16x8*)(lds + PG8_SA(b, h) + aoff + m * 2048 + k * 1024); } } } while (0)
; #define PG8_LDB(dst, b, h) do { _Pragma("unroll") for (int n = 0; n < 2; ++n) { if constexpr (F8) dst##8[n] = PG8_LD32(lds + PG8_SB(b, h) + boff + n * 2048); \
;         else { _Pragma("unroll") for (int k = 0; k < 2; ++k) dst[n][k] = *(const LAS bf16x8*)(lds + PG8_SB(b, h) + boff + n * 2048 + k * 1024); } } } while (0)
; #define PG8_WAIT_V(n) asm volatile("s_waitcnt vmcnt(" #n ")" ::: "memory")
; #define PG8_WAIT_L(n) asm volatile("s_waitcnt lgkmcnt(" #n ")" ::: "memory")
; #define PG8_BAR __builtin_amdgcn_s_barrier()
; #define PG8_SCHED __builtin_amdgcn_sched_barrier(0)
; template <class Epi, class Sched, bool GATHER, bool F8 = false>
; __device__ __forceinline__ void gemm_phase(LAS unsigned char* lds, const int K, const Sched& S, const Epi& E) {
;     ...
;             PG8_LDB(B0, 1, 0); PG8_LDB(B1, 1, 1); PG8_SCHED; PG8_LDA(At, 1, 0); PG8_STAGE(PG8_SA(0, 1), a2, vN[1]);
;             PG8_WAIT_V(8); PG8_WAIT_L(0); PG8_BAR; PG8_MMA(0, 0, At, B0); PG8_MMA(0, 1, At, B1); PG8_BAR; PG8_SCHED;
;             PG8_LDA(At, 1, 1); PG8_STAGE(PG8_SB(1, 0), b3, voffB); PG8_STAGE(PG8_SB(1, 1), b3 + hstepB, voffB); PG8_STAGE(PG8_SA(1, 0), a3, vN[0]);
;             PG8_WAIT_V(8); PG8_WAIT_L(0); PG8_BAR; PG8_MMA(1, 0, At, B0); PG8_MMA(1, 1, At, B1); PG8_BAR; PG8_SCHED;
;         }
;         if (wr == 0) PG8_BAR;
	s_add_i32 s84, 0, 0x18000
	s_add_i32 s85, 0, 0x1c000
	v_add_u32_e32 v14, s84, v171
	v_add_u32_e32 v30, s85, v171
	ds_read_b128 v[2:5], v14
	ds_read_b128 v[6:9], v14 offset:1024
	ds_read_b128 v[10:13], v14 offset:2048
	ds_read_b128 v[14:17], v14 offset:3072
	ds_read_b128 v[18:21], v30
	ds_read_b128 v[22:25], v30 offset:1024
	ds_read_b128 v[26:29], v30 offset:2048
	ds_read_b128 v[30:33], v30 offset:3072
	s_mov_b32 m0, s68
	v_lshl_add_u64 v[244:245], s[62:63], 0, v[166:167]
	ds_read_b128 v[212:215], v208 offset:32768
	ds_read_b128 v[216:219], v208 offset:33792
	ds_read_b128 v[220:223], v208 offset:34816
	ds_read_b128 v[224:227], v208 offset:35840
	ds_read_b128 v[228:231], v208 offset:36864
	ds_read_b128 v[232:235], v208 offset:37888
	ds_read_b128 v[236:239], v208 offset:38912
	ds_read_b128 v[240:243], v208 offset:39936
	global_load_lds_dwordx4 v[244:245], off
	v_lshl_add_u64 v[244:245], s[62:63], 0, v[174:175]
	s_mov_b32 m0, s69
	s_nop 0
	global_load_lds_dwordx4 v[244:245], off
	s_waitcnt vmcnt(8)
	s_waitcnt lgkmcnt(0)
	s_barrier
	s_setprio 1
	s_waitcnt lgkmcnt(0)
	v_mfma_scale_f32_16x16x128_f8f6f4 v[158:161], v[2:9], v[212:219], v[158:161], v190, v190 op_sel_hi:[0,0,0]
	v_mfma_scale_f32_16x16x128_f8f6f4 v[154:157], v[10:17], v[212:219], v[154:157], v190, v190 op_sel_hi:[0,0,0]
	v_mfma_scale_f32_16x16x128_f8f6f4 v[142:145], v[2:9], v[220:227], v[142:145], v190, v190 op_sel_hi:[0,0,0]
	v_mfma_scale_f32_16x16x128_f8f6f4 v[138:141], v[10:17], v[220:227], v[138:141], v190, v190 op_sel_hi:[0,0,0]
	v_mfma_scale_f32_16x16x128_f8f6f4 v[126:129], v[2:9], v[228:235], v[126:129], v190, v190 op_sel_hi:[0,0,0]
	v_mfma_scale_f32_16x16x128_f8f6f4 v[122:125], v[10:17], v[228:235], v[122:125], v190, v190 op_sel_hi:[0,0,0]
	v_mfma_scale_f32_16x16x128_f8f6f4 v[110:113], v[2:9], v[236:243], v[110:113], v190, v190 op_sel_hi:[0,0,0]
	v_mfma_scale_f32_16x16x128_f8f6f4 v[106:109], v[10:17], v[236:243], v[106:109], v190, v190 op_sel_hi:[0,0,0]
	s_setprio 0
	s_setprio 1
	v_mfma_scale_f32_16x16x128_f8f6f4 v[150:153], v[18:25], v[212:219], v[150:153], v190, v190 op_sel_hi:[0,0,0]
	v_mfma_scale_f32_16x16x128_f8f6f4 v[146:149], v[26:33], v[212:219], v[146:149], v190, v190 op_sel_hi:[0,0,0]
	v_mfma_scale_f32_16x16x128_f8f6f4 v[134:137], v[18:25], v[220:227], v[134:137], v190, v190 op_sel_hi:[0,0,0]
	v_mfma_scale_f32_16x16x128_f8f6f4 v[130:133], v[26:33], v[220:227], v[130:133], v190, v190 op_sel_hi:[0,0,0]
	v_mfma_scale_f32_16x16x128_f8f6f4 v[118:121], v[18:25], v[228:235], v[118:121], v190, v190 op_sel_hi:[0,0,0]
	v_mfma_scale_f32_16x16x128_f8f6f4 v[114:117], v[26:33], v[228:235], v[114:117], v190, v190 op_sel_hi:[0,0,0]
	v_mfma_scale_f32_16x16x128_f8f6f4 v[102:105], v[18:25], v[236:243], v[102:105], v190, v190 op_sel_hi:[0,0,0]
	v_mfma_scale_f32_16x16x128_f8f6f4 v[98:101], v[26:33], v[236:243], v[98:101], v190, v190 op_sel_hi:[0,0,0]
	s_setprio 0
	s_barrier
	s_add_i32 s62, s84, s65
	v_lshl_add_u64 v[182:183], v[182:183], 0, s[20:21]
	s_mov_b32 m0, s62
	ds_read_b128 v[212:215], v208 offset:49152
	ds_read_b128 v[216:219], v208 offset:50176
	ds_read_b128 v[220:223], v208 offset:51200
	ds_read_b128 v[224:227], v208 offset:52224
	ds_read_b128 v[228:231], v208 offset:53248
	ds_read_b128 v[232:235], v208 offset:54272
	ds_read_b128 v[236:239], v208 offset:55296
	ds_read_b128 v[240:243], v208 offset:56320
	global_load_lds_dwordx4 v[182:183], off
	s_add_i32 m0, s62, 0x2000
	s_add_u32 s48, s48, 0x10080
	v_lshl_add_u64 v[182:183], v[184:185], 0, s[20:21]
	s_addc_u32 s49, s49, 0
	s_add_i32 s62, s85, s65
	global_load_lds_dwordx4 v[182:183], off
	v_lshl_add_u64 v[182:183], s[48:49], 0, v[162:163]
	s_mov_b32 m0, s62
	s_nop 0
	global_load_lds_dwordx4 v[182:183], off
	v_lshl_add_u64 v[182:183], s[48:49], 0, v[168:169]
	s_add_i32 m0, s62, 0x2000
	s_nop 0
	global_load_lds_dwordx4 v[182:183], off
	v_lshl_add_u64 v[182:183], v[186:187], 0, s[20:21]
	s_mov_b32 m0, s72
	s_nop 0
	global_load_lds_dwordx4 v[182:183], off
	v_lshl_add_u64 v[182:183], v[188:189], 0, s[20:21]
	s_mov_b32 m0, s73
	s_nop 0
	global_load_lds_dwordx4 v[182:183], off
	s_waitcnt vmcnt(8)
	s_waitcnt lgkmcnt(0)
	s_barrier
	s_setprio 1
	s_waitcnt lgkmcnt(0)
	v_mfma_scale_f32_16x16x128_f8f6f4 v[94:97], v[2:9], v[212:219], v[94:97], v190, v190 op_sel_hi:[0,0,0]
	v_mfma_scale_f32_16x16x128_f8f6f4 v[90:93], v[10:17], v[212:219], v[90:93], v190, v190 op_sel_hi:[0,0,0]
	v_mfma_scale_f32_16x16x128_f8f6f4 v[78:81], v[2:9], v[220:227], v[78:81], v190, v190 op_sel_hi:[0,0,0]
	v_mfma_scale_f32_16x16x128_f8f6f4 v[74:77], v[10:17], v[220:227], v[74:77], v190, v190 op_sel_hi:[0,0,0]
	v_mfma_scale_f32_16x16x128_f8f6f4 v[62:65], v[2:9], v[228:235], v[62:65], v190, v190 op_sel_hi:[0,0,0]
	v_mfma_scale_f32_16x16x128_f8f6f4 v[58:61], v[10:17], v[228:235], v[58:61], v190, v190 op_sel_hi:[0,0,0]
	v_mfma_scale_f32_16x16x128_f8f6f4 v[46:49], v[2:9], v[236:243], v[46:49], v190, v190 op_sel_hi:[0,0,0]
	v_mfma_scale_f32_16x16x128_f8f6f4 v[42:45], v[10:17], v[236:243], v[42:45], v190, v190 op_sel_hi:[0,0,0]
	s_setprio 0
	s_setprio 1
	v_mfma_scale_f32_16x16x128_f8f6f4 v[86:89], v[18:25], v[212:219], v[86:89], v190, v190 op_sel_hi:[0,0,0]
	v_mfma_scale_f32_16x16x128_f8f6f4 v[82:85], v[26:33], v[212:219], v[82:85], v190, v190 op_sel_hi:[0,0,0]
	v_mfma_scale_f32_16x16x128_f8f6f4 v[70:73], v[18:25], v[220:227], v[70:73], v190, v190 op_sel_hi:[0,0,0]
	v_mfma_scale_f32_16x16x128_f8f6f4 v[66:69], v[26:33], v[220:227], v[66:69], v190, v190 op_sel_hi:[0,0,0]
	v_mfma_scale_f32_16x16x128_f8f6f4 v[54:57], v[18:25], v[228:235], v[54:57], v190, v190 op_sel_hi:[0,0,0]
	v_mfma_scale_f32_16x16x128_f8f6f4 v[50:53], v[26:33], v[228:235], v[50:53], v190, v190 op_sel_hi:[0,0,0]
	v_mfma_scale_f32_16x16x128_f8f6f4 v[38:41], v[18:25], v[236:243], v[38:41], v190, v190 op_sel_hi:[0,0,0]
	v_mfma_scale_f32_16x16x128_f8f6f4 v[34:37], v[26:33], v[236:243], v[34:37], v190, v190 op_sel_hi:[0,0,0]
	s_setprio 0
	s_barrier
	s_add_i32 s97, s97, 2
	s_add_u32 s46, s46, 0x100
	s_addc_u32 s47, s47, 0
	s_add_u32 s95, s95, 0x100
	s_addc_u32 s96, s96, 0
	s_cmp_gt_u32 s97, 13
	s_cbranch_scc0 .LBB0_346
	s_and_b64 vcc, exec, s[24:25]
	s_cbranch_vccz .LBB0_349
	s_barrier

; #define PG8_STAGE(bufoff, gbase, voff) do { _Pragma("unroll") for (int _i = 0; _i < 2; ++_i) \
;         __builtin_amdgcn_global_load_lds((const unsigned*)((const char*)(gbase) + (voff)[_i]), (LAS unsigned*)(lds + (bufoff) + ldsw + _i * 8192), 16, 0, 0); } while (0)
; #define PG8_LDA(dst, b, h) do { _Pragma("unroll") for (int m = 0; m < 4; ++m) { if constexpr (F8) dst##8[m] = PG8_LD32(lds + PG8_SA(b, h) + aoff + m * 2048); \
;         else { _Pragma("unroll") for (int k = 0; k < 2; ++k) dst[m][k] = *(const LAS bf16x8*)(lds + PG8_SA(b, h) + aoff + m * 2048 + k * 1024); } } } while (0)
; #define PG8_LDB(dst, b, h) do { _Pragma("unroll") for (int n = 0; n < 2; ++n) { if constexpr (F8) dst##8[n] = PG8_LD32(lds + PG8_SB(b, h) + boff + n * 2048); \
;         else { _Pragma("unroll") for (int k = 0; k < 2; ++k) dst[n][k] = *(const LAS bf16x8*)(lds + PG8_SB(b, h) + boff + n * 2048 + k * 1024); } } } while (0)
; #define PG8_WAIT_V(n) asm volatile("s_waitcnt vmcnt(" #n ")" ::: "memory")
; #define PG8_WAIT_L(n) asm volatile("s_waitcnt lgkmcnt(" #n ")" ::: "memory")
; #define PG8_BAR __builtin_amdgcn_s_barrier()
; #define PG8_SCHED __builtin_amdgcn_sched_barrier(0)
; template <class Epi, class Sched, bool GATHER, bool F8 = false>
; __device__ __forceinline__ void gemm_phase(LAS unsigned char* lds, const int K, const Sched& S, const Epi& E) {
;     ...
;             PG8_LDB(B0, 0, 0); PG8_LDB(B1, 0, 1); PG8_SCHED; PG8_LDA(At, 0, 0); PG8_STAGE(PG8_SA(1, 1), a1, vA[1]);
;             PG8_WAIT_V(8); PG8_WAIT_L(0); PG8_BAR; PG8_MMA(0, 0, At, B0); PG8_MMA(0, 1, At, B1); PG8_BAR; PG8_SCHED;
;             PG8_LDA(At, 0, 1); PG8_STAGE(PG8_SB(0, 0), b2, voffB); PG8_STAGE(PG8_SB(0, 1), b2 + hstepB, voffB); PG8_STAGE(PG8_SA(0, 0), a2, vN[0]);
;             PG8_WAIT_V(8); PG8_WAIT_L(0); PG8_BAR; PG8_MMA(1, 0, At, B0); PG8_MMA(1, 1, At, B1); PG8_BAR; PG8_SCHED;
.LBB0_558:
	v_add_u32_e32 v156, s74, v165
	ds_read_b128 v[2:5], v156
	ds_read_b128 v[6:9], v156 offset:1024
	ds_read_b128 v[182:185], v156 offset:2048
	ds_read_b128 v[186:189], v156 offset:3072
	v_add_u32_e32 v156, s75, v165
	ds_read_b128 v[190:193], v156
	ds_read_b128 v[194:197], v156 offset:1024
	ds_read_b128 v[198:201], v156 offset:2048
	ds_read_b128 v[202:205], v156 offset:3072
	s_add_u32 s60, s4, 0x80
	s_addc_u32 s61, s5, 0
	s_cmp_eq_u32 s55, 4
	s_cselect_b32 s63, s57, s61
	s_cselect_b32 s62, s56, s60
	s_cselect_b32 s61, s53, s7
	s_cselect_b32 s60, s52, s6
	v_lshl_add_u64 v[230:231], s[4:5], 0, v[152:153]
	s_add_i32 m0, s66, 0xc000
	ds_read_b128 v[156:159], v179
	ds_read_b128 v[160:163], v179 offset:1024
	ds_read_b128 v[206:209], v179 offset:2048
	ds_read_b128 v[210:213], v179 offset:3072
	ds_read_b128 v[214:217], v179 offset:4096
	ds_read_b128 v[218:221], v179 offset:5120
	ds_read_b128 v[222:225], v179 offset:6144
	ds_read_b128 v[226:229], v179 offset:7168
	global_load_lds_dwordx4 v[230:231], off
	v_lshl_add_u64 v[230:231], s[4:5], 0, v[154:155]
	s_add_i32 m0, s66, 0xe000
	s_nop 0
	global_load_lds_dwordx4 v[230:231], off
	s_waitcnt vmcnt(8)
	s_waitcnt lgkmcnt(0)
	s_barrier
	s_setprio 1
	s_waitcnt lgkmcnt(0)
	v_mfma_scale_f32_16x16x128_f8f6f4 v[134:137], v[2:9], v[156:163], v[134:137], v1, v1 op_sel_hi:[0,0,0]
	v_mfma_scale_f32_16x16x128_f8f6f4 v[130:133], v[182:189], v[156:163], v[130:133], v1, v1 op_sel_hi:[0,0,0]
	v_mfma_scale_f32_16x16x128_f8f6f4 v[126:129], v[2:9], v[206:213], v[126:129], v1, v1 op_sel_hi:[0,0,0]
	v_mfma_scale_f32_16x16x128_f8f6f4 v[122:125], v[182:189], v[206:213], v[122:125], v1, v1 op_sel_hi:[0,0,0]
	v_mfma_scale_f32_16x16x128_f8f6f4 v[118:121], v[2:9], v[214:221], v[118:121], v1, v1 op_sel_hi:[0,0,0]
	v_mfma_scale_f32_16x16x128_f8f6f4 v[114:117], v[182:189], v[214:221], v[114:117], v1, v1 op_sel_hi:[0,0,0]
	v_mfma_scale_f32_16x16x128_f8f6f4 v[110:113], v[2:9], v[222:229], v[110:113], v1, v1 op_sel_hi:[0,0,0]
	v_mfma_scale_f32_16x16x128_f8f6f4 v[106:109], v[182:189], v[222:229], v[106:109], v1, v1 op_sel_hi:[0,0,0]
	s_setprio 0
	s_setprio 1
	v_mfma_scale_f32_16x16x128_f8f6f4 v[102:105], v[190:197], v[156:163], v[102:105], v1, v1 op_sel_hi:[0,0,0]
	v_mfma_scale_f32_16x16x128_f8f6f4 v[98:101], v[198:205], v[156:163], v[98:101], v1, v1 op_sel_hi:[0,0,0]
	v_mfma_scale_f32_16x16x128_f8f6f4 v[94:97], v[190:197], v[206:213], v[94:97], v1, v1 op_sel_hi:[0,0,0]
	v_mfma_scale_f32_16x16x128_f8f6f4 v[90:93], v[198:205], v[206:213], v[90:93], v1, v1 op_sel_hi:[0,0,0]
	v_mfma_scale_f32_16x16x128_f8f6f4 v[86:89], v[190:197], v[214:221], v[86:89], v1, v1 op_sel_hi:[0,0,0]
	v_mfma_scale_f32_16x16x128_f8f6f4 v[82:85], v[198:205], v[214:221], v[82:85], v1, v1 op_sel_hi:[0,0,0]
	v_mfma_scale_f32_16x16x128_f8f6f4 v[78:81], v[190:197], v[222:229], v[78:81], v1, v1 op_sel_hi:[0,0,0]
	v_mfma_scale_f32_16x16x128_f8f6f4 v[74:77], v[198:205], v[222:229], v[74:77], v1, v1 op_sel_hi:[0,0,0]
	s_setprio 0
	s_barrier
	s_add_i32 s77, s74, s65
	v_lshl_add_u64 v[156:157], s[60:61], 0, v[138:139]
	s_mov_b32 m0, s77
	ds_read_b128 v[206:209], v179 offset:16384
	ds_read_b128 v[210:213], v179 offset:17408
	ds_read_b128 v[214:217], v179 offset:18432
	ds_read_b128 v[218:221], v179 offset:19456
	ds_read_b128 v[222:225], v179 offset:20480
	ds_read_b128 v[226:229], v179 offset:21504
	ds_read_b128 v[230:233], v179 offset:22528
	ds_read_b128 v[234:237], v179 offset:23552
	global_load_lds_dwordx4 v[156:157], off
	s_add_i32 m0, s77, 0x2000
	s_add_u32 s78, s60, 0x8000
	v_lshl_add_u64 v[158:159], s[60:61], 0, v[144:145]
	s_addc_u32 s79, s61, 0
	s_add_i32 s77, s75, s65
	global_load_lds_dwordx4 v[158:159], off
	v_lshl_add_u64 v[160:161], s[78:79], 0, v[138:139]
	s_mov_b32 m0, s77
	v_lshl_add_u64 v[162:163], s[62:63], 0, v[146:147]
	global_load_lds_dwordx4 v[160:161], off
	v_lshl_add_u64 v[160:161], s[78:79], 0, v[144:145]
	s_add_i32 m0, s77, 0x2000
	s_nop 0
	global_load_lds_dwordx4 v[160:161], off
	v_lshl_add_u64 v[160:161], s[62:63], 0, v[140:141]
	s_mov_b32 m0, s66
	s_nop 0
	global_load_lds_dwordx4 v[160:161], off
	s_mov_b32 m0, s67
	s_nop 0
	global_load_lds_dwordx4 v[162:163], off
	s_nop 0
	s_waitcnt vmcnt(8)
	s_waitcnt lgkmcnt(0)
	s_barrier
	s_setprio 1
	s_waitcnt lgkmcnt(0)
	v_mfma_scale_f32_16x16x128_f8f6f4 v[70:73], v[2:9], v[206:213], v[70:73], v1, v1 op_sel_hi:[0,0,0]
	v_mfma_scale_f32_16x16x128_f8f6f4 v[66:69], v[182:189], v[206:213], v[66:69], v1, v1 op_sel_hi:[0,0,0]
	v_mfma_scale_f32_16x16x128_f8f6f4 v[62:65], v[2:9], v[214:221], v[62:65], v1, v1 op_sel_hi:[0,0,0]
	v_mfma_scale_f32_16x16x128_f8f6f4 v[58:61], v[182:189], v[214:221], v[58:61], v1, v1 op_sel_hi:[0,0,0]
	v_mfma_scale_f32_16x16x128_f8f6f4 v[54:57], v[2:9], v[222:229], v[54:57], v1, v1 op_sel_hi:[0,0,0]
	v_mfma_scale_f32_16x16x128_f8f6f4 v[50:53], v[182:189], v[222:229], v[50:53], v1, v1 op_sel_hi:[0,0,0]
	v_mfma_scale_f32_16x16x128_f8f6f4 v[46:49], v[2:9], v[230:237], v[46:49], v1, v1 op_sel_hi:[0,0,0]
	v_mfma_scale_f32_16x16x128_f8f6f4 v[42:45], v[182:189], v[230:237], v[42:45], v1, v1 op_sel_hi:[0,0,0]
	s_setprio 0
	s_setprio 1
	v_mfma_scale_f32_16x16x128_f8f6f4 v[38:41], v[190:197], v[206:213], v[38:41], v1, v1 op_sel_hi:[0,0,0]
	v_mfma_scale_f32_16x16x128_f8f6f4 v[34:37], v[198:205], v[206:213], v[34:37], v1, v1 op_sel_hi:[0,0,0]
	v_mfma_scale_f32_16x16x128_f8f6f4 v[30:33], v[190:197], v[214:221], v[30:33], v1, v1 op_sel_hi:[0,0,0]
	v_mfma_scale_f32_16x16x128_f8f6f4 v[26:29], v[198:205], v[214:221], v[26:29], v1, v1 op_sel_hi:[0,0,0]
	v_mfma_scale_f32_16x16x128_f8f6f4 v[22:25], v[190:197], v[222:229], v[22:25], v1, v1 op_sel_hi:[0,0,0]
	v_mfma_scale_f32_16x16x128_f8f6f4 v[18:21], v[198:205], v[222:229], v[18:21], v1, v1 op_sel_hi:[0,0,0]
	v_mfma_scale_f32_16x16x128_f8f6f4 v[14:17], v[190:197], v[230:237], v[14:17], v1, v1 op_sel_hi:[0,0,0]
	v_mfma_scale_f32_16x16x128_f8f6f4 v[10:13], v[198:205], v[230:237], v[10:13], v1, v1 op_sel_hi:[0,0,0]
	s_setprio 0
	s_barrier
; #define PG8_STAGE(bufoff, gbase, voff) do { _Pragma("unroll") for (int _i = 0; _i < 2; ++_i) \
;         __builtin_amdgcn_global_load_lds((const unsigned*)((const char*)(gbase) + (voff)[_i]), (LAS unsigned*)(lds + (bufoff) + ldsw + _i * 8192), 16, 0, 0); } while (0)
; #define PG8_LDA(dst, b, h) do { _Pragma("unroll") for (int m = 0; m < 4; ++m) { if constexpr (F8) dst##8[m] = PG8_LD32(lds + PG8_SA(b, h) + aoff + m * 2048); \
;         else { _Pragma("unroll") for (int k = 0; k < 2; ++k) dst[m][k] = *(const LAS bf16x8*)(lds + PG8_SA(b, h) + aoff + m * 2048 + k * 1024); } } } while (0)
; #define PG8_LDB(dst, b, h) do { _Pragma("unroll") for (int n = 0; n < 2; ++n) { if constexpr (F8) dst##8[n] = PG8_LD32(lds + PG8_SB(b, h) + boff + n * 2048); \
;         else { _Pragma("unroll") for (int k = 0; k < 2; ++k) dst[n][k] = *(const LAS bf16x8*)(lds + PG8_SB(b, h) + boff + n * 2048 + k * 1024); } } } while (0)
; #define PG8_WAIT_V(n) asm volatile("s_waitcnt vmcnt(" #n ")" ::: "memory")
; #define PG8_WAIT_L(n) asm volatile("s_waitcnt lgkmcnt(" #n ")" ::: "memory")
; #define PG8_BAR __builtin_amdgcn_s_barrier()
; #define PG8_SCHED __builtin_amdgcn_sched_barrier(0)
; template <class Epi, class Sched, bool GATHER, bool F8 = false>
; __device__ __forceinline__ void gemm_phase(LAS unsigned char* lds, const int K, const Sched& S, const Epi& E) {
;     ...
;             PG8_LDB(B0, 1, 0); PG8_LDB(B1, 1, 1); PG8_SCHED; PG8_LDA(At, 1, 0); PG8_STAGE(PG8_SA(0, 1), a2, vN[1]);
;             PG8_WAIT_V(8); PG8_WAIT_L(0); PG8_BAR; PG8_MMA(0, 0, At, B0); PG8_MMA(0, 1, At, B1); PG8_BAR; PG8_SCHED;
;             PG8_LDA(At, 1, 1); PG8_STAGE(PG8_SB(1, 0), b3, voffB); PG8_STAGE(PG8_SB(1, 1), b3 + hstepB, voffB); PG8_STAGE(PG8_SA(1, 0), a3, vN[0]);
;             PG8_WAIT_V(8); PG8_WAIT_L(0); PG8_BAR; PG8_MMA(1, 0, At, B0); PG8_MMA(1, 1, At, B1); PG8_BAR; PG8_SCHED;
;         }
;         if (wr == 0) PG8_BAR;
	s_add_i32 s77, 0, 0x18000
	s_add_i32 s78, 0, 0x1c000
	v_add_u32_e32 v2, s77, v165
	v_add_u32_e32 v181, s78, v165
	ds_read_b128 v[182:185], v2
	ds_read_b128 v[186:189], v2 offset:1024
	ds_read_b128 v[190:193], v2 offset:2048
	ds_read_b128 v[194:197], v2 offset:3072
	ds_read_b128 v[2:5], v181
	ds_read_b128 v[6:9], v181 offset:1024
	ds_read_b128 v[198:201], v181 offset:2048
	ds_read_b128 v[202:205], v181 offset:3072
	s_mov_b32 m0, s68
	v_lshl_add_u64 v[238:239], s[62:63], 0, v[142:143]
	ds_read_b128 v[206:209], v179 offset:32768
	ds_read_b128 v[210:213], v179 offset:33792
	ds_read_b128 v[214:217], v179 offset:34816
	ds_read_b128 v[218:221], v179 offset:35840
	ds_read_b128 v[222:225], v179 offset:36864
	ds_read_b128 v[226:229], v179 offset:37888
	ds_read_b128 v[230:233], v179 offset:38912
	ds_read_b128 v[234:237], v179 offset:39936
	global_load_lds_dwordx4 v[238:239], off
	v_lshl_add_u64 v[238:239], s[62:63], 0, v[148:149]
	s_mov_b32 m0, s69
	s_nop 0
	global_load_lds_dwordx4 v[238:239], off
	s_waitcnt vmcnt(8)
	s_waitcnt lgkmcnt(0)
	s_barrier
	s_setprio 1
	s_waitcnt lgkmcnt(0)
	v_mfma_scale_f32_16x16x128_f8f6f4 v[134:137], v[182:189], v[206:213], v[134:137], v1, v1 op_sel_hi:[0,0,0]
	v_mfma_scale_f32_16x16x128_f8f6f4 v[130:133], v[190:197], v[206:213], v[130:133], v1, v1 op_sel_hi:[0,0,0]
	v_mfma_scale_f32_16x16x128_f8f6f4 v[126:129], v[182:189], v[214:221], v[126:129], v1, v1 op_sel_hi:[0,0,0]
	v_mfma_scale_f32_16x16x128_f8f6f4 v[122:125], v[190:197], v[214:221], v[122:125], v1, v1 op_sel_hi:[0,0,0]
	v_mfma_scale_f32_16x16x128_f8f6f4 v[118:121], v[182:189], v[222:229], v[118:121], v1, v1 op_sel_hi:[0,0,0]
	v_mfma_scale_f32_16x16x128_f8f6f4 v[114:117], v[190:197], v[222:229], v[114:117], v1, v1 op_sel_hi:[0,0,0]
	v_mfma_scale_f32_16x16x128_f8f6f4 v[110:113], v[182:189], v[230:237], v[110:113], v1, v1 op_sel_hi:[0,0,0]
	v_mfma_scale_f32_16x16x128_f8f6f4 v[106:109], v[190:197], v[230:237], v[106:109], v1, v1 op_sel_hi:[0,0,0]
	s_setprio 0
	s_setprio 1
	v_mfma_scale_f32_16x16x128_f8f6f4 v[102:105], v[2:9], v[206:213], v[102:105], v1, v1 op_sel_hi:[0,0,0]
	v_mfma_scale_f32_16x16x128_f8f6f4 v[98:101], v[198:205], v[206:213], v[98:101], v1, v1 op_sel_hi:[0,0,0]
	v_mfma_scale_f32_16x16x128_f8f6f4 v[94:97], v[2:9], v[214:221], v[94:97], v1, v1 op_sel_hi:[0,0,0]
	v_mfma_scale_f32_16x16x128_f8f6f4 v[90:93], v[198:205], v[214:221], v[90:93], v1, v1 op_sel_hi:[0,0,0]
	v_mfma_scale_f32_16x16x128_f8f6f4 v[86:89], v[2:9], v[222:229], v[86:89], v1, v1 op_sel_hi:[0,0,0]
	v_mfma_scale_f32_16x16x128_f8f6f4 v[82:85], v[198:205], v[222:229], v[82:85], v1, v1 op_sel_hi:[0,0,0]
	v_mfma_scale_f32_16x16x128_f8f6f4 v[78:81], v[2:9], v[230:237], v[78:81], v1, v1 op_sel_hi:[0,0,0]
	v_mfma_scale_f32_16x16x128_f8f6f4 v[74:77], v[198:205], v[230:237], v[74:77], v1, v1 op_sel_hi:[0,0,0]
	s_setprio 0
	s_barrier
	s_add_i32 s62, s77, s65
	v_lshl_add_u64 v[156:157], v[156:157], 0, s[42:43]
	s_mov_b32 m0, s62
	ds_read_b128 v[206:209], v179 offset:49152
	ds_read_b128 v[210:213], v179 offset:50176
	ds_read_b128 v[214:217], v179 offset:51200
	ds_read_b128 v[218:221], v179 offset:52224
	ds_read_b128 v[222:225], v179 offset:53248
	ds_read_b128 v[226:229], v179 offset:54272
	ds_read_b128 v[230:233], v179 offset:55296
	ds_read_b128 v[234:237], v179 offset:56320
	global_load_lds_dwordx4 v[156:157], off
	s_add_i32 m0, s62, 0x2000
	s_add_u32 s60, s60, 0x8080
	v_lshl_add_u64 v[156:157], v[158:159], 0, s[42:43]
	s_addc_u32 s61, s61, 0
	s_add_i32 s62, s78, s65
	global_load_lds_dwordx4 v[156:157], off
	v_lshl_add_u64 v[156:157], s[60:61], 0, v[138:139]
	s_mov_b32 m0, s62
	s_nop 0
	global_load_lds_dwordx4 v[156:157], off
	v_lshl_add_u64 v[156:157], s[60:61], 0, v[144:145]
	s_add_i32 m0, s62, 0x2000
	s_nop 0
	global_load_lds_dwordx4 v[156:157], off
	v_lshl_add_u64 v[156:157], v[160:161], 0, s[42:43]
	s_mov_b32 m0, s70
	s_nop 0
	global_load_lds_dwordx4 v[156:157], off
	v_lshl_add_u64 v[156:157], v[162:163], 0, s[42:43]
	s_mov_b32 m0, s71
	s_nop 0
	global_load_lds_dwordx4 v[156:157], off
	s_waitcnt vmcnt(8)
	s_waitcnt lgkmcnt(0)
	s_barrier
	s_setprio 1
	s_waitcnt lgkmcnt(0)
	v_mfma_scale_f32_16x16x128_f8f6f4 v[70:73], v[182:189], v[206:213], v[70:73], v1, v1 op_sel_hi:[0,0,0]
	v_mfma_scale_f32_16x16x128_f8f6f4 v[66:69], v[190:197], v[206:213], v[66:69], v1, v1 op_sel_hi:[0,0,0]
	v_mfma_scale_f32_16x16x128_f8f6f4 v[62:65], v[182:189], v[214:221], v[62:65], v1, v1 op_sel_hi:[0,0,0]
	v_mfma_scale_f32_16x16x128_f8f6f4 v[58:61], v[190:197], v[214:221], v[58:61], v1, v1 op_sel_hi:[0,0,0]
	v_mfma_scale_f32_16x16x128_f8f6f4 v[54:57], v[182:189], v[222:229], v[54:57], v1, v1 op_sel_hi:[0,0,0]
	v_mfma_scale_f32_16x16x128_f8f6f4 v[50:53], v[190:197], v[222:229], v[50:53], v1, v1 op_sel_hi:[0,0,0]
	v_mfma_scale_f32_16x16x128_f8f6f4 v[46:49], v[182:189], v[230:237], v[46:49], v1, v1 op_sel_hi:[0,0,0]
	v_mfma_scale_f32_16x16x128_f8f6f4 v[42:45], v[190:197], v[230:237], v[42:45], v1, v1 op_sel_hi:[0,0,0]
	s_setprio 0
	s_setprio 1
	v_mfma_scale_f32_16x16x128_f8f6f4 v[38:41], v[2:9], v[206:213], v[38:41], v1, v1 op_sel_hi:[0,0,0]
	v_mfma_scale_f32_16x16x128_f8f6f4 v[34:37], v[198:205], v[206:213], v[34:37], v1, v1 op_sel_hi:[0,0,0]
	v_mfma_scale_f32_16x16x128_f8f6f4 v[30:33], v[2:9], v[214:221], v[30:33], v1, v1 op_sel_hi:[0,0,0]
	v_mfma_scale_f32_16x16x128_f8f6f4 v[26:29], v[198:205], v[214:221], v[26:29], v1, v1 op_sel_hi:[0,0,0]
	v_mfma_scale_f32_16x16x128_f8f6f4 v[22:25], v[2:9], v[222:229], v[22:25], v1, v1 op_sel_hi:[0,0,0]
	v_mfma_scale_f32_16x16x128_f8f6f4 v[18:21], v[198:205], v[222:229], v[18:21], v1, v1 op_sel_hi:[0,0,0]
	v_mfma_scale_f32_16x16x128_f8f6f4 v[14:17], v[2:9], v[230:237], v[14:17], v1, v1 op_sel_hi:[0,0,0]
	v_mfma_scale_f32_16x16x128_f8f6f4 v[10:13], v[198:205], v[230:237], v[10:13], v1, v1 op_sel_hi:[0,0,0]
	s_setprio 0
	s_barrier
	s_add_i32 s55, s55, 2
	s_add_u32 s4, s4, 0x100
	s_addc_u32 s5, s5, 0
	s_add_u32 s6, s6, 0x100
	s_addc_u32 s7, s7, 0
	s_cmp_gt_u32 s55, 5
	s_cbranch_scc0 .LBB0_558
	s_and_b64 vcc, exec, s[44:45]
	s_cbranch_vccz .LBB0_561
	s_barrier

; #define PG8_STAGE(bufoff, gbase, voff) do { _Pragma("unroll") for (int _i = 0; _i < 2; ++_i) \
;         __builtin_amdgcn_global_load_lds((const unsigned*)((const char*)(gbase) + (voff)[_i]), (LAS unsigned*)(lds + (bufoff) + ldsw + _i * 8192), 16, 0, 0); } while (0)
; #define PG8_LDA(dst, b, h) do { _Pragma("unroll") for (int m = 0; m < 4; ++m) { if constexpr (F8) dst##8[m] = PG8_LD32(lds + PG8_SA(b, h) + aoff + m * 2048); \
;         else { _Pragma("unroll") for (int k = 0; k < 2; ++k) dst[m][k] = *(const LAS bf16x8*)(lds + PG8_SA(b, h) + aoff + m * 2048 + k * 1024); } } } while (0)
; #define PG8_LDB(dst, b, h) do { _Pragma("unroll") for (int n = 0; n < 2; ++n) { if constexpr (F8) dst##8[n] = PG8_LD32(lds + PG8_SB(b, h) + boff + n * 2048); \
;         else { _Pragma("unroll") for (int k = 0; k < 2; ++k) dst[n][k] = *(const LAS bf16x8*)(lds + PG8_SB(b, h) + boff + n * 2048 + k * 1024); } } } while (0)
; #define PG8_WAIT_V(n) asm volatile("s_waitcnt vmcnt(" #n ")" ::: "memory")
; #define PG8_WAIT_L(n) asm volatile("s_waitcnt lgkmcnt(" #n ")" ::: "memory")
; #define PG8_BAR __builtin_amdgcn_s_barrier()
; #define PG8_SCHED __builtin_amdgcn_sched_barrier(0)
; template <class Epi, class Sched, bool GATHER, bool F8 = false>
; __device__ __forceinline__ void gemm_phase(LAS unsigned char* lds, const int K, const Sched& S, const Epi& E) {
;     ...
;             PG8_LDB(B0, 0, 0); PG8_LDB(B1, 0, 1); PG8_SCHED; PG8_LDA(At, 0, 0); PG8_STAGE(PG8_SA(1, 1), a1, vA[1]);
;             PG8_WAIT_V(8); PG8_WAIT_L(0); PG8_BAR; PG8_MMA(0, 0, At, B0); PG8_MMA(0, 1, At, B1); PG8_BAR; PG8_SCHED;
;             PG8_LDA(At, 0, 1); PG8_STAGE(PG8_SB(0, 0), b2, voffB); PG8_STAGE(PG8_SB(0, 1), b2 + hstepB, voffB); PG8_STAGE(PG8_SA(0, 0), a2, vN[0]);
;             PG8_WAIT_V(8); PG8_WAIT_L(0); PG8_BAR; PG8_MMA(1, 0, At, B0); PG8_MMA(1, 1, At, B1); PG8_BAR; PG8_SCHED;
.LBB0_702:
	ds_read_b128 v[18:21], v191
	ds_read_b128 v[22:25], v191 offset:1024
	ds_read_b128 v[26:29], v191 offset:2048
	ds_read_b128 v[30:33], v191 offset:3072
	ds_read_b128 v[2:5], v192
	ds_read_b128 v[6:9], v192 offset:1024
	ds_read_b128 v[10:13], v192 offset:2048
	ds_read_b128 v[14:17], v192 offset:3072
	s_add_u32 s42, s38, s40
	s_addc_u32 s43, s39, s41
	s_add_u32 s42, s42, 0x2f200100
	s_addc_u32 s43, s43, 0
	s_add_u32 s63, s50, s40
	s_addc_u32 s64, s51, s41
	s_cmpk_eq_i32 s40, 0x700
	s_cselect_b32 s45, s17, s43
	s_cselect_b32 s44, s16, s42
	s_cselect_b32 s43, s21, s64
	s_cselect_b32 s42, s20, s63
	s_mov_b32 m0, s53
	v_lshl_add_u64 v[220:221], v[176:177], 0, s[40:41]
	ds_read_b128 v[180:183], v193
	ds_read_b128 v[184:187], v193 offset:1024
	ds_read_b128 v[196:199], v193 offset:2048
	ds_read_b128 v[200:203], v193 offset:3072
	ds_read_b128 v[204:207], v193 offset:4096
	ds_read_b128 v[208:211], v193 offset:5120
	ds_read_b128 v[212:215], v193 offset:6144
	ds_read_b128 v[216:219], v193 offset:7168
	global_load_lds_dwordx4 v[220:221], off
	v_lshl_add_u64 v[220:221], v[178:179], 0, s[40:41]
	s_mov_b32 m0, s54
	s_nop 0
	global_load_lds_dwordx4 v[220:221], off
	s_waitcnt vmcnt(8)
	s_waitcnt lgkmcnt(0)
	s_barrier
	s_setprio 1
	s_waitcnt lgkmcnt(0)
	v_mfma_scale_f32_16x16x128_f8f6f4 v[158:161], v[18:25], v[180:187], v[158:161], v188, v188 op_sel_hi:[0,0,0]
	v_mfma_scale_f32_16x16x128_f8f6f4 v[154:157], v[26:33], v[180:187], v[154:157], v188, v188 op_sel_hi:[0,0,0]
	v_mfma_scale_f32_16x16x128_f8f6f4 v[142:145], v[18:25], v[196:203], v[142:145], v188, v188 op_sel_hi:[0,0,0]
	v_mfma_scale_f32_16x16x128_f8f6f4 v[138:141], v[26:33], v[196:203], v[138:141], v188, v188 op_sel_hi:[0,0,0]
	v_mfma_scale_f32_16x16x128_f8f6f4 v[126:129], v[18:25], v[204:211], v[126:129], v188, v188 op_sel_hi:[0,0,0]
	v_mfma_scale_f32_16x16x128_f8f6f4 v[122:125], v[26:33], v[204:211], v[122:125], v188, v188 op_sel_hi:[0,0,0]
	v_mfma_scale_f32_16x16x128_f8f6f4 v[110:113], v[18:25], v[212:219], v[110:113], v188, v188 op_sel_hi:[0,0,0]
	v_mfma_scale_f32_16x16x128_f8f6f4 v[106:109], v[26:33], v[212:219], v[106:109], v188, v188 op_sel_hi:[0,0,0]
	s_setprio 0
	s_setprio 1
	v_mfma_scale_f32_16x16x128_f8f6f4 v[150:153], v[2:9], v[180:187], v[150:153], v188, v188 op_sel_hi:[0,0,0]
	v_mfma_scale_f32_16x16x128_f8f6f4 v[146:149], v[10:17], v[180:187], v[146:149], v188, v188 op_sel_hi:[0,0,0]
	v_mfma_scale_f32_16x16x128_f8f6f4 v[134:137], v[2:9], v[196:203], v[134:137], v188, v188 op_sel_hi:[0,0,0]
	v_mfma_scale_f32_16x16x128_f8f6f4 v[130:133], v[10:17], v[196:203], v[130:133], v188, v188 op_sel_hi:[0,0,0]
	v_mfma_scale_f32_16x16x128_f8f6f4 v[118:121], v[2:9], v[204:211], v[118:121], v188, v188 op_sel_hi:[0,0,0]
	v_mfma_scale_f32_16x16x128_f8f6f4 v[114:117], v[10:17], v[204:211], v[114:117], v188, v188 op_sel_hi:[0,0,0]
	v_mfma_scale_f32_16x16x128_f8f6f4 v[102:105], v[2:9], v[212:219], v[102:105], v188, v188 op_sel_hi:[0,0,0]
	v_mfma_scale_f32_16x16x128_f8f6f4 v[98:101], v[10:17], v[212:219], v[98:101], v188, v188 op_sel_hi:[0,0,0]
	s_setprio 0
	s_barrier
	s_mov_b32 m0, s55
	v_lshl_add_u64 v[180:181], s[42:43], 0, v[162:163]
	s_add_u32 s64, s42, 0x10000
	ds_read_b128 v[196:199], v193 offset:16384
	ds_read_b128 v[200:203], v193 offset:17408
	ds_read_b128 v[204:207], v193 offset:18432
	ds_read_b128 v[208:211], v193 offset:19456
	ds_read_b128 v[212:215], v193 offset:20480
	ds_read_b128 v[216:219], v193 offset:21504
	ds_read_b128 v[220:223], v193 offset:22528
	ds_read_b128 v[224:227], v193 offset:23552
	global_load_lds_dwordx4 v[180:181], off
	v_lshl_add_u64 v[182:183], s[42:43], 0, v[168:169]
	s_mov_b32 m0, s56
	s_addc_u32 s65, s43, 0
	global_load_lds_dwordx4 v[182:183], off
	v_lshl_add_u64 v[184:185], s[64:65], 0, v[162:163]
	s_mov_b32 m0, s57
	v_lshl_add_u64 v[186:187], s[44:45], 0, v[172:173]
	global_load_lds_dwordx4 v[184:185], off
	v_lshl_add_u64 v[184:185], s[64:65], 0, v[168:169]
	s_mov_b32 m0, s58
	s_nop 0
	global_load_lds_dwordx4 v[184:185], off
	v_lshl_add_u64 v[184:185], s[44:45], 0, v[164:165]
	s_mov_b32 m0, s1
	s_nop 0
	global_load_lds_dwordx4 v[184:185], off
	s_mov_b32 m0, s6
	s_nop 0
	global_load_lds_dwordx4 v[186:187], off
	s_nop 0
	s_waitcnt vmcnt(8)
	s_waitcnt lgkmcnt(0)
	s_barrier
	s_setprio 1
	s_waitcnt lgkmcnt(0)
	v_mfma_scale_f32_16x16x128_f8f6f4 v[94:97], v[18:25], v[196:203], v[94:97], v188, v188 op_sel_hi:[0,0,0]
	v_mfma_scale_f32_16x16x128_f8f6f4 v[90:93], v[26:33], v[196:203], v[90:93], v188, v188 op_sel_hi:[0,0,0]
	v_mfma_scale_f32_16x16x128_f8f6f4 v[78:81], v[18:25], v[204:211], v[78:81], v188, v188 op_sel_hi:[0,0,0]
	v_mfma_scale_f32_16x16x128_f8f6f4 v[74:77], v[26:33], v[204:211], v[74:77], v188, v188 op_sel_hi:[0,0,0]
	v_mfma_scale_f32_16x16x128_f8f6f4 v[62:65], v[18:25], v[212:219], v[62:65], v188, v188 op_sel_hi:[0,0,0]
	v_mfma_scale_f32_16x16x128_f8f6f4 v[58:61], v[26:33], v[212:219], v[58:61], v188, v188 op_sel_hi:[0,0,0]
	v_mfma_scale_f32_16x16x128_f8f6f4 v[46:49], v[18:25], v[220:227], v[46:49], v188, v188 op_sel_hi:[0,0,0]
	v_mfma_scale_f32_16x16x128_f8f6f4 v[42:45], v[26:33], v[220:227], v[42:45], v188, v188 op_sel_hi:[0,0,0]
	s_setprio 0
	s_setprio 1
	v_mfma_scale_f32_16x16x128_f8f6f4 v[86:89], v[2:9], v[196:203], v[86:89], v188, v188 op_sel_hi:[0,0,0]
	v_mfma_scale_f32_16x16x128_f8f6f4 v[82:85], v[10:17], v[196:203], v[82:85], v188, v188 op_sel_hi:[0,0,0]
	v_mfma_scale_f32_16x16x128_f8f6f4 v[70:73], v[2:9], v[204:211], v[70:73], v188, v188 op_sel_hi:[0,0,0]
	v_mfma_scale_f32_16x16x128_f8f6f4 v[66:69], v[10:17], v[204:211], v[66:69], v188, v188 op_sel_hi:[0,0,0]
	v_mfma_scale_f32_16x16x128_f8f6f4 v[54:57], v[2:9], v[212:219], v[54:57], v188, v188 op_sel_hi:[0,0,0]
	v_mfma_scale_f32_16x16x128_f8f6f4 v[50:53], v[10:17], v[212:219], v[50:53], v188, v188 op_sel_hi:[0,0,0]
	v_mfma_scale_f32_16x16x128_f8f6f4 v[38:41], v[2:9], v[220:227], v[38:41], v188, v188 op_sel_hi:[0,0,0]
	v_mfma_scale_f32_16x16x128_f8f6f4 v[34:37], v[10:17], v[220:227], v[34:37], v188, v188 op_sel_hi:[0,0,0]
	s_setprio 0
	s_barrier
; #define PG8_STAGE(bufoff, gbase, voff) do { _Pragma("unroll") for (int _i = 0; _i < 2; ++_i) \
;         __builtin_amdgcn_global_load_lds((const unsigned*)((const char*)(gbase) + (voff)[_i]), (LAS unsigned*)(lds + (bufoff) + ldsw + _i * 8192), 16, 0, 0); } while (0)
; #define PG8_LDA(dst, b, h) do { _Pragma("unroll") for (int m = 0; m < 4; ++m) { if constexpr (F8) dst##8[m] = PG8_LD32(lds + PG8_SA(b, h) + aoff + m * 2048); \
;         else { _Pragma("unroll") for (int k = 0; k < 2; ++k) dst[m][k] = *(const LAS bf16x8*)(lds + PG8_SA(b, h) + aoff + m * 2048 + k * 1024); } } } while (0)
; #define PG8_LDB(dst, b, h) do { _Pragma("unroll") for (int n = 0; n < 2; ++n) { if constexpr (F8) dst##8[n] = PG8_LD32(lds + PG8_SB(b, h) + boff + n * 2048); \
;         else { _Pragma("unroll") for (int k = 0; k < 2; ++k) dst[n][k] = *(const LAS bf16x8*)(lds + PG8_SB(b, h) + boff + n * 2048 + k * 1024); } } } while (0)
; #define PG8_WAIT_V(n) asm volatile("s_waitcnt vmcnt(" #n ")" ::: "memory")
; #define PG8_WAIT_L(n) asm volatile("s_waitcnt lgkmcnt(" #n ")" ::: "memory")
; #define PG8_BAR __builtin_amdgcn_s_barrier()
; #define PG8_SCHED __builtin_amdgcn_sched_barrier(0)
; template <class Epi, class Sched, bool GATHER, bool F8 = false>
; __device__ __forceinline__ void gemm_phase(LAS unsigned char* lds, const int K, const Sched& S, const Epi& E) {
;     ...
;             PG8_LDB(B0, 1, 0); PG8_LDB(B1, 1, 1); PG8_SCHED; PG8_LDA(At, 1, 0); PG8_STAGE(PG8_SA(0, 1), a2, vN[1]);
;             PG8_WAIT_V(8); PG8_WAIT_L(0); PG8_BAR; PG8_MMA(0, 0, At, B0); PG8_MMA(0, 1, At, B1); PG8_BAR; PG8_SCHED;
;             PG8_LDA(At, 1, 1); PG8_STAGE(PG8_SB(1, 0), b3, voffB); PG8_STAGE(PG8_SB(1, 1), b3 + hstepB, voffB); PG8_STAGE(PG8_SA(1, 0), a3, vN[0]);
;             PG8_WAIT_V(8); PG8_WAIT_L(0); PG8_BAR; PG8_MMA(1, 0, At, B0); PG8_MMA(1, 1, At, B1); PG8_BAR; PG8_SCHED;
;         }
;         if (wr == 0) PG8_BAR;
	ds_read_b128 v[2:5], v194
	ds_read_b128 v[6:9], v194 offset:1024
	ds_read_b128 v[10:13], v194 offset:2048
	ds_read_b128 v[14:17], v194 offset:3072
	ds_read_b128 v[18:21], v195
	ds_read_b128 v[22:25], v195 offset:1024
	ds_read_b128 v[26:29], v195 offset:2048
	ds_read_b128 v[30:33], v195 offset:3072
	s_mov_b32 m0, s13
	v_lshl_add_u64 v[228:229], s[44:45], 0, v[166:167]
	ds_read_b128 v[196:199], v193 offset:32768
	ds_read_b128 v[200:203], v193 offset:33792
	ds_read_b128 v[204:207], v193 offset:34816
	ds_read_b128 v[208:211], v193 offset:35840
	ds_read_b128 v[212:215], v193 offset:36864
	ds_read_b128 v[216:219], v193 offset:37888
	ds_read_b128 v[220:223], v193 offset:38912
	ds_read_b128 v[224:227], v193 offset:39936
	global_load_lds_dwordx4 v[228:229], off
	v_lshl_add_u64 v[228:229], s[44:45], 0, v[174:175]
	s_mov_b32 m0, s46
	s_nop 0
	global_load_lds_dwordx4 v[228:229], off
	s_waitcnt vmcnt(8)
	s_waitcnt lgkmcnt(0)
	s_barrier
	s_setprio 1
	s_waitcnt lgkmcnt(0)
	v_mfma_scale_f32_16x16x128_f8f6f4 v[158:161], v[2:9], v[196:203], v[158:161], v188, v188 op_sel_hi:[0,0,0]
	v_mfma_scale_f32_16x16x128_f8f6f4 v[154:157], v[10:17], v[196:203], v[154:157], v188, v188 op_sel_hi:[0,0,0]
	v_mfma_scale_f32_16x16x128_f8f6f4 v[142:145], v[2:9], v[204:211], v[142:145], v188, v188 op_sel_hi:[0,0,0]
	v_mfma_scale_f32_16x16x128_f8f6f4 v[138:141], v[10:17], v[204:211], v[138:141], v188, v188 op_sel_hi:[0,0,0]
	v_mfma_scale_f32_16x16x128_f8f6f4 v[126:129], v[2:9], v[212:219], v[126:129], v188, v188 op_sel_hi:[0,0,0]
	v_mfma_scale_f32_16x16x128_f8f6f4 v[122:125], v[10:17], v[212:219], v[122:125], v188, v188 op_sel_hi:[0,0,0]
	v_mfma_scale_f32_16x16x128_f8f6f4 v[110:113], v[2:9], v[220:227], v[110:113], v188, v188 op_sel_hi:[0,0,0]
	v_mfma_scale_f32_16x16x128_f8f6f4 v[106:109], v[10:17], v[220:227], v[106:109], v188, v188 op_sel_hi:[0,0,0]
	s_setprio 0
	s_setprio 1
	v_mfma_scale_f32_16x16x128_f8f6f4 v[150:153], v[18:25], v[196:203], v[150:153], v188, v188 op_sel_hi:[0,0,0]
	v_mfma_scale_f32_16x16x128_f8f6f4 v[146:149], v[26:33], v[196:203], v[146:149], v188, v188 op_sel_hi:[0,0,0]
	v_mfma_scale_f32_16x16x128_f8f6f4 v[134:137], v[18:25], v[204:211], v[134:137], v188, v188 op_sel_hi:[0,0,0]
	v_mfma_scale_f32_16x16x128_f8f6f4 v[130:133], v[26:33], v[204:211], v[130:133], v188, v188 op_sel_hi:[0,0,0]
	v_mfma_scale_f32_16x16x128_f8f6f4 v[118:121], v[18:25], v[212:219], v[118:121], v188, v188 op_sel_hi:[0,0,0]
	v_mfma_scale_f32_16x16x128_f8f6f4 v[114:117], v[26:33], v[212:219], v[114:117], v188, v188 op_sel_hi:[0,0,0]
	v_mfma_scale_f32_16x16x128_f8f6f4 v[102:105], v[18:25], v[220:227], v[102:105], v188, v188 op_sel_hi:[0,0,0]
	v_mfma_scale_f32_16x16x128_f8f6f4 v[98:101], v[26:33], v[220:227], v[98:101], v188, v188 op_sel_hi:[0,0,0]
	s_setprio 0
	s_barrier
	s_mov_b32 m0, s59
	v_lshl_add_u64 v[180:181], v[180:181], 0, s[24:25]
	s_add_u32 s42, s42, 0x10080
	ds_read_b128 v[196:199], v193 offset:49152
	ds_read_b128 v[200:203], v193 offset:50176
	ds_read_b128 v[204:207], v193 offset:51200
	ds_read_b128 v[208:211], v193 offset:52224
	ds_read_b128 v[212:215], v193 offset:53248
	ds_read_b128 v[216:219], v193 offset:54272
	ds_read_b128 v[220:223], v193 offset:55296
	ds_read_b128 v[224:227], v193 offset:56320
	global_load_lds_dwordx4 v[180:181], off
	v_lshl_add_u64 v[180:181], v[182:183], 0, s[24:25]
	s_mov_b32 m0, s60
	s_addc_u32 s43, s43, 0
	global_load_lds_dwordx4 v[180:181], off
	v_lshl_add_u64 v[180:181], s[42:43], 0, v[162:163]
	s_mov_b32 m0, s61
	s_nop 0
	global_load_lds_dwordx4 v[180:181], off
	v_lshl_add_u64 v[180:181], s[42:43], 0, v[168:169]
	s_mov_b32 m0, s62
	s_nop 0
	global_load_lds_dwordx4 v[180:181], off
	v_lshl_add_u64 v[180:181], v[184:185], 0, s[24:25]
	s_mov_b32 m0, s48
	s_nop 0
	global_load_lds_dwordx4 v[180:181], off
	v_lshl_add_u64 v[180:181], v[186:187], 0, s[24:25]
	s_mov_b32 m0, s49
	s_nop 0
	global_load_lds_dwordx4 v[180:181], off
	s_waitcnt vmcnt(8)
	s_waitcnt lgkmcnt(0)
	s_barrier
	s_setprio 1
	s_waitcnt lgkmcnt(0)
	v_mfma_scale_f32_16x16x128_f8f6f4 v[94:97], v[2:9], v[196:203], v[94:97], v188, v188 op_sel_hi:[0,0,0]
	v_mfma_scale_f32_16x16x128_f8f6f4 v[90:93], v[10:17], v[196:203], v[90:93], v188, v188 op_sel_hi:[0,0,0]
	v_mfma_scale_f32_16x16x128_f8f6f4 v[78:81], v[2:9], v[204:211], v[78:81], v188, v188 op_sel_hi:[0,0,0]
	v_mfma_scale_f32_16x16x128_f8f6f4 v[74:77], v[10:17], v[204:211], v[74:77], v188, v188 op_sel_hi:[0,0,0]
	v_mfma_scale_f32_16x16x128_f8f6f4 v[62:65], v[2:9], v[212:219], v[62:65], v188, v188 op_sel_hi:[0,0,0]
	v_mfma_scale_f32_16x16x128_f8f6f4 v[58:61], v[10:17], v[212:219], v[58:61], v188, v188 op_sel_hi:[0,0,0]
	v_mfma_scale_f32_16x16x128_f8f6f4 v[46:49], v[2:9], v[220:227], v[46:49], v188, v188 op_sel_hi:[0,0,0]
	v_mfma_scale_f32_16x16x128_f8f6f4 v[42:45], v[10:17], v[220:227], v[42:45], v188, v188 op_sel_hi:[0,0,0]
	s_setprio 0
	s_setprio 1
	v_mfma_scale_f32_16x16x128_f8f6f4 v[86:89], v[18:25], v[196:203], v[86:89], v188, v188 op_sel_hi:[0,0,0]
	v_mfma_scale_f32_16x16x128_f8f6f4 v[82:85], v[26:33], v[196:203], v[82:85], v188, v188 op_sel_hi:[0,0,0]
	v_mfma_scale_f32_16x16x128_f8f6f4 v[70:73], v[18:25], v[204:211], v[70:73], v188, v188 op_sel_hi:[0,0,0]
	v_mfma_scale_f32_16x16x128_f8f6f4 v[66:69], v[26:33], v[204:211], v[66:69], v188, v188 op_sel_hi:[0,0,0]
	v_mfma_scale_f32_16x16x128_f8f6f4 v[54:57], v[18:25], v[212:219], v[54:57], v188, v188 op_sel_hi:[0,0,0]
	v_mfma_scale_f32_16x16x128_f8f6f4 v[50:53], v[26:33], v[212:219], v[50:53], v188, v188 op_sel_hi:[0,0,0]
	v_mfma_scale_f32_16x16x128_f8f6f4 v[38:41], v[18:25], v[220:227], v[38:41], v188, v188 op_sel_hi:[0,0,0]
	v_mfma_scale_f32_16x16x128_f8f6f4 v[34:37], v[26:33], v[220:227], v[34:37], v188, v188 op_sel_hi:[0,0,0]
	s_setprio 0
	s_barrier
	s_add_i32 s52, s52, 2
	s_add_u32 s40, s40, 0x100
	s_addc_u32 s41, s41, 0
	s_cmp_gt_u32 s52, 13
	s_cbranch_scc0 .LBB0_702
	s_cmpk_lt_u32 s3, 0x100
	s_cbranch_scc0 .LBB0_705
	s_barrier

; #define PG8_STAGE(bufoff, gbase, voff) do { _Pragma("unroll") for (int _i = 0; _i < 2; ++_i) \
;         __builtin_amdgcn_global_load_lds((const unsigned*)((const char*)(gbase) + (voff)[_i]), (LAS unsigned*)(lds + (bufoff) + ldsw + _i * 8192), 16, 0, 0); } while (0)
; #define PG8_LDA(dst, b, h) do { _Pragma("unroll") for (int m = 0; m < 4; ++m) { if constexpr (F8) dst##8[m] = PG8_LD32(lds + PG8_SA(b, h) + aoff + m * 2048); \
;         else { _Pragma("unroll") for (int k = 0; k < 2; ++k) dst[m][k] = *(const LAS bf16x8*)(lds + PG8_SA(b, h) + aoff + m * 2048 + k * 1024); } } } while (0)
; #define PG8_LDB(dst, b, h) do { _Pragma("unroll") for (int n = 0; n < 2; ++n) { if constexpr (F8) dst##8[n] = PG8_LD32(lds + PG8_SB(b, h) + boff + n * 2048); \
;         else { _Pragma("unroll") for (int k = 0; k < 2; ++k) dst[n][k] = *(const LAS bf16x8*)(lds + PG8_SB(b, h) + boff + n * 2048 + k * 1024); } } } while (0)
; #define PG8_WAIT_V(n) asm volatile("s_waitcnt vmcnt(" #n ")" ::: "memory")
; #define PG8_WAIT_L(n) asm volatile("s_waitcnt lgkmcnt(" #n ")" ::: "memory")
; #define PG8_BAR __builtin_amdgcn_s_barrier()
; #define PG8_SCHED __builtin_amdgcn_sched_barrier(0)
; template <class Epi, class Sched, bool GATHER, bool F8 = false>
; __device__ __forceinline__ void gemm_phase(LAS unsigned char* lds, const int K, const Sched& S, const Epi& E) {
;     ...
;             PG8_LDB(B0, 0, 0); PG8_LDB(B1, 0, 1); PG8_SCHED; PG8_LDA(At, 0, 0); PG8_STAGE(PG8_SA(1, 1), a1, vA[1]);
;             PG8_WAIT_V(8); PG8_WAIT_L(0); PG8_BAR; PG8_MMA(0, 0, At, B0); PG8_MMA(0, 1, At, B1); PG8_BAR; PG8_SCHED;
;             PG8_LDA(At, 0, 1); PG8_STAGE(PG8_SB(0, 0), b2, voffB); PG8_STAGE(PG8_SB(0, 1), b2 + hstepB, voffB); PG8_STAGE(PG8_SA(0, 0), a2, vN[0]);
;             PG8_WAIT_V(8); PG8_WAIT_L(0); PG8_BAR; PG8_MMA(1, 0, At, B0); PG8_MMA(1, 1, At, B1); PG8_BAR; PG8_SCHED;
.LBB0_1128:
	v_add_u32_e32 v74, s60, v163
	ds_read_b128 v[2:5], v74
	ds_read_b128 v[6:9], v74 offset:1024
	ds_read_b128 v[172:175], v74 offset:2048
	ds_read_b128 v[176:179], v74 offset:3072
	v_add_u32_e32 v74, s61, v163
	ds_read_b128 v[180:183], v74
	ds_read_b128 v[184:187], v74 offset:1024
	ds_read_b128 v[188:191], v74 offset:2048
	ds_read_b128 v[192:195], v74 offset:3072
	s_add_u32 s46, s44, 0x80
	s_addc_u32 s47, s45, 0
	s_cmp_eq_u32 s18, 12
	s_cselect_b32 s49, s41, s47
	s_cselect_b32 s48, s40, s46
	s_cselect_b32 s47, s43, s13
	s_cselect_b32 s46, s42, s1
	v_lshl_add_u64 v[220:221], s[44:45], 0, v[158:159]
	s_add_i32 m0, s51, 0xc000
	ds_read_b128 v[74:77], v167
	ds_read_b128 v[78:81], v167 offset:1024
	ds_read_b128 v[196:199], v167 offset:2048
	ds_read_b128 v[200:203], v167 offset:3072
	ds_read_b128 v[204:207], v167 offset:4096
	ds_read_b128 v[208:211], v167 offset:5120
	ds_read_b128 v[212:215], v167 offset:6144
	ds_read_b128 v[216:219], v167 offset:7168
	global_load_lds_dwordx4 v[220:221], off
	v_lshl_add_u64 v[220:221], s[44:45], 0, v[160:161]
	s_add_i32 m0, s51, 0xe000
	s_nop 0
	global_load_lds_dwordx4 v[220:221], off
	s_nop 0
	s_waitcnt vmcnt(8)
	s_waitcnt lgkmcnt(0)
	s_barrier
	s_setprio 1
	s_waitcnt lgkmcnt(0)
	v_mfma_scale_f32_16x16x128_f8f6f4 v[142:145], v[2:9], v[74:81], v[142:145], v162, v162 op_sel_hi:[0,0,0]
	v_mfma_scale_f32_16x16x128_f8f6f4 v[138:141], v[172:179], v[74:81], v[138:141], v162, v162 op_sel_hi:[0,0,0]
	v_mfma_scale_f32_16x16x128_f8f6f4 v[126:129], v[2:9], v[196:203], v[126:129], v162, v162 op_sel_hi:[0,0,0]
	v_mfma_scale_f32_16x16x128_f8f6f4 v[122:125], v[172:179], v[196:203], v[122:125], v162, v162 op_sel_hi:[0,0,0]
	v_mfma_scale_f32_16x16x128_f8f6f4 v[110:113], v[2:9], v[204:211], v[110:113], v162, v162 op_sel_hi:[0,0,0]
	v_mfma_scale_f32_16x16x128_f8f6f4 v[106:109], v[172:179], v[204:211], v[106:109], v162, v162 op_sel_hi:[0,0,0]
	v_mfma_scale_f32_16x16x128_f8f6f4 v[94:97], v[2:9], v[212:219], v[94:97], v162, v162 op_sel_hi:[0,0,0]
	v_mfma_scale_f32_16x16x128_f8f6f4 v[90:93], v[172:179], v[212:219], v[90:93], v162, v162 op_sel_hi:[0,0,0]
	s_setprio 0
	s_setprio 1
	v_mfma_scale_f32_16x16x128_f8f6f4 v[134:137], v[180:187], v[74:81], v[134:137], v162, v162 op_sel_hi:[0,0,0]
	v_mfma_scale_f32_16x16x128_f8f6f4 v[130:133], v[188:195], v[74:81], v[130:133], v162, v162 op_sel_hi:[0,0,0]
	v_mfma_scale_f32_16x16x128_f8f6f4 v[118:121], v[180:187], v[196:203], v[118:121], v162, v162 op_sel_hi:[0,0,0]
	v_mfma_scale_f32_16x16x128_f8f6f4 v[114:117], v[188:195], v[196:203], v[114:117], v162, v162 op_sel_hi:[0,0,0]
	v_mfma_scale_f32_16x16x128_f8f6f4 v[102:105], v[180:187], v[204:211], v[102:105], v162, v162 op_sel_hi:[0,0,0]
	v_mfma_scale_f32_16x16x128_f8f6f4 v[98:101], v[188:195], v[204:211], v[98:101], v162, v162 op_sel_hi:[0,0,0]
	v_mfma_scale_f32_16x16x128_f8f6f4 v[86:89], v[180:187], v[212:219], v[86:89], v162, v162 op_sel_hi:[0,0,0]
	v_mfma_scale_f32_16x16x128_f8f6f4 v[82:85], v[188:195], v[212:219], v[82:85], v162, v162 op_sel_hi:[0,0,0]
	s_setprio 0
	s_barrier
	s_add_i32 s65, s60, s25
	v_lshl_add_u64 v[74:75], s[46:47], 0, v[156:157]
	s_mov_b32 m0, s65
	ds_read_b128 v[196:199], v167 offset:16384
	ds_read_b128 v[200:203], v167 offset:17408
	ds_read_b128 v[204:207], v167 offset:18432
	ds_read_b128 v[208:211], v167 offset:19456
	ds_read_b128 v[212:215], v167 offset:20480
	ds_read_b128 v[216:219], v167 offset:21504
	ds_read_b128 v[220:223], v167 offset:22528
	ds_read_b128 v[224:227], v167 offset:23552
	global_load_lds_dwordx4 v[74:75], off
	s_add_i32 m0, s65, 0x2000
	s_add_u32 s66, s46, 0x10000
	v_lshl_add_u64 v[76:77], s[46:47], 0, v[150:151]
	s_addc_u32 s67, s47, 0
	s_add_i32 s65, s61, s25
	global_load_lds_dwordx4 v[76:77], off
	v_lshl_add_u64 v[78:79], s[66:67], 0, v[156:157]
	s_mov_b32 m0, s65
	v_lshl_add_u64 v[80:81], s[48:49], 0, v[146:147]
	global_load_lds_dwordx4 v[78:79], off
	v_lshl_add_u64 v[78:79], s[66:67], 0, v[150:151]
	s_add_i32 m0, s65, 0x2000
	s_nop 0
	global_load_lds_dwordx4 v[78:79], off
	v_lshl_add_u64 v[78:79], s[48:49], 0, v[152:153]
	s_mov_b32 m0, s51
	s_nop 0
	global_load_lds_dwordx4 v[78:79], off
	s_mov_b32 m0, s52
	s_nop 0
	global_load_lds_dwordx4 v[80:81], off
	s_nop 0
	s_waitcnt vmcnt(8)
	s_waitcnt lgkmcnt(0)
	s_barrier
	s_setprio 1
	s_waitcnt lgkmcnt(0)
	v_mfma_scale_f32_16x16x128_f8f6f4 v[70:73], v[2:9], v[196:203], v[70:73], v162, v162 op_sel_hi:[0,0,0]
	v_mfma_scale_f32_16x16x128_f8f6f4 v[66:69], v[172:179], v[196:203], v[66:69], v162, v162 op_sel_hi:[0,0,0]
	v_mfma_scale_f32_16x16x128_f8f6f4 v[54:57], v[2:9], v[204:211], v[54:57], v162, v162 op_sel_hi:[0,0,0]
	v_mfma_scale_f32_16x16x128_f8f6f4 v[50:53], v[172:179], v[204:211], v[50:53], v162, v162 op_sel_hi:[0,0,0]
	v_mfma_scale_f32_16x16x128_f8f6f4 v[38:41], v[2:9], v[212:219], v[38:41], v162, v162 op_sel_hi:[0,0,0]
	v_mfma_scale_f32_16x16x128_f8f6f4 v[34:37], v[172:179], v[212:219], v[34:37], v162, v162 op_sel_hi:[0,0,0]
	v_mfma_scale_f32_16x16x128_f8f6f4 v[18:21], v[2:9], v[220:227], v[18:21], v162, v162 op_sel_hi:[0,0,0]
	v_mfma_scale_f32_16x16x128_f8f6f4 v[22:25], v[172:179], v[220:227], v[22:25], v162, v162 op_sel_hi:[0,0,0]
	s_setprio 0
	s_setprio 1
	v_mfma_scale_f32_16x16x128_f8f6f4 v[62:65], v[180:187], v[196:203], v[62:65], v162, v162 op_sel_hi:[0,0,0]
	v_mfma_scale_f32_16x16x128_f8f6f4 v[58:61], v[188:195], v[196:203], v[58:61], v162, v162 op_sel_hi:[0,0,0]
	v_mfma_scale_f32_16x16x128_f8f6f4 v[46:49], v[180:187], v[204:211], v[46:49], v162, v162 op_sel_hi:[0,0,0]
	v_mfma_scale_f32_16x16x128_f8f6f4 v[42:45], v[188:195], v[204:211], v[42:45], v162, v162 op_sel_hi:[0,0,0]
	v_mfma_scale_f32_16x16x128_f8f6f4 v[30:33], v[180:187], v[212:219], v[30:33], v162, v162 op_sel_hi:[0,0,0]
	v_mfma_scale_f32_16x16x128_f8f6f4 v[26:29], v[188:195], v[212:219], v[26:29], v162, v162 op_sel_hi:[0,0,0]
	v_mfma_scale_f32_16x16x128_f8f6f4 v[10:13], v[180:187], v[220:227], v[10:13], v162, v162 op_sel_hi:[0,0,0]
	v_mfma_scale_f32_16x16x128_f8f6f4 v[14:17], v[188:195], v[220:227], v[14:17], v162, v162 op_sel_hi:[0,0,0]
	s_setprio 0
	s_barrier
; #define PG8_STAGE(bufoff, gbase, voff) do { _Pragma("unroll") for (int _i = 0; _i < 2; ++_i) \
;         __builtin_amdgcn_global_load_lds((const unsigned*)((const char*)(gbase) + (voff)[_i]), (LAS unsigned*)(lds + (bufoff) + ldsw + _i * 8192), 16, 0, 0); } while (0)
; #define PG8_LDA(dst, b, h) do { _Pragma("unroll") for (int m = 0; m < 4; ++m) { if constexpr (F8) dst##8[m] = PG8_LD32(lds + PG8_SA(b, h) + aoff + m * 2048); \
;         else { _Pragma("unroll") for (int k = 0; k < 2; ++k) dst[m][k] = *(const LAS bf16x8*)(lds + PG8_SA(b, h) + aoff + m * 2048 + k * 1024); } } } while (0)
; #define PG8_LDB(dst, b, h) do { _Pragma("unroll") for (int n = 0; n < 2; ++n) { if constexpr (F8) dst##8[n] = PG8_LD32(lds + PG8_SB(b, h) + boff + n * 2048); \
;         else { _Pragma("unroll") for (int k = 0; k < 2; ++k) dst[n][k] = *(const LAS bf16x8*)(lds + PG8_SB(b, h) + boff + n * 2048 + k * 1024); } } } while (0)
; #define PG8_WAIT_V(n) asm volatile("s_waitcnt vmcnt(" #n ")" ::: "memory")
; #define PG8_WAIT_L(n) asm volatile("s_waitcnt lgkmcnt(" #n ")" ::: "memory")
; #define PG8_BAR __builtin_amdgcn_s_barrier()
; #define PG8_SCHED __builtin_amdgcn_sched_barrier(0)
; template <class Epi, class Sched, bool GATHER, bool F8 = false>
; __device__ __forceinline__ void gemm_phase(LAS unsigned char* lds, const int K, const Sched& S, const Epi& E) {
;     ...
;             PG8_LDB(B0, 1, 0); PG8_LDB(B1, 1, 1); PG8_SCHED; PG8_LDA(At, 1, 0); PG8_STAGE(PG8_SA(0, 1), a2, vN[1]);
;             PG8_WAIT_V(8); PG8_WAIT_L(0); PG8_BAR; PG8_MMA(0, 0, At, B0); PG8_MMA(0, 1, At, B1); PG8_BAR; PG8_SCHED;
;             PG8_LDA(At, 1, 1); PG8_STAGE(PG8_SB(1, 0), b3, voffB); PG8_STAGE(PG8_SB(1, 1), b3 + hstepB, voffB); PG8_STAGE(PG8_SA(1, 0), a3, vN[0]);
;             PG8_WAIT_V(8); PG8_WAIT_L(0); PG8_BAR; PG8_MMA(1, 0, At, B0); PG8_MMA(1, 1, At, B1); PG8_BAR; PG8_SCHED;
;         }
;         if (wr == 0) PG8_BAR;
	s_add_i32 s65, 0, 0x18000
	s_add_i32 s66, 0, 0x1c000
	v_add_u32_e32 v2, s65, v163
	v_add_u32_e32 v192, s66, v163
	ds_read_b128 v[172:175], v2
	ds_read_b128 v[176:179], v2 offset:1024
	ds_read_b128 v[180:183], v2 offset:2048
	ds_read_b128 v[184:187], v2 offset:3072
	ds_read_b128 v[2:5], v192
	ds_read_b128 v[6:9], v192 offset:1024
	ds_read_b128 v[188:191], v192 offset:2048
	ds_read_b128 v[192:195], v192 offset:3072
	s_mov_b32 m0, s53
	v_lshl_add_u64 v[228:229], s[48:49], 0, v[154:155]
	ds_read_b128 v[196:199], v167 offset:32768
	ds_read_b128 v[200:203], v167 offset:33792
	ds_read_b128 v[204:207], v167 offset:34816
	ds_read_b128 v[208:211], v167 offset:35840
	ds_read_b128 v[212:215], v167 offset:36864
	ds_read_b128 v[216:219], v167 offset:37888
	ds_read_b128 v[220:223], v167 offset:38912
	ds_read_b128 v[224:227], v167 offset:39936
	global_load_lds_dwordx4 v[228:229], off
	v_lshl_add_u64 v[228:229], s[48:49], 0, v[148:149]
	s_mov_b32 m0, s54
	s_nop 0
	global_load_lds_dwordx4 v[228:229], off
	s_waitcnt vmcnt(8)
	s_waitcnt lgkmcnt(0)
	s_barrier
	s_setprio 1
	s_waitcnt lgkmcnt(0)
	v_mfma_scale_f32_16x16x128_f8f6f4 v[142:145], v[172:179], v[196:203], v[142:145], v162, v162 op_sel_hi:[0,0,0]
	v_mfma_scale_f32_16x16x128_f8f6f4 v[138:141], v[180:187], v[196:203], v[138:141], v162, v162 op_sel_hi:[0,0,0]
	v_mfma_scale_f32_16x16x128_f8f6f4 v[126:129], v[172:179], v[204:211], v[126:129], v162, v162 op_sel_hi:[0,0,0]
	v_mfma_scale_f32_16x16x128_f8f6f4 v[122:125], v[180:187], v[204:211], v[122:125], v162, v162 op_sel_hi:[0,0,0]
	v_mfma_scale_f32_16x16x128_f8f6f4 v[110:113], v[172:179], v[212:219], v[110:113], v162, v162 op_sel_hi:[0,0,0]
	v_mfma_scale_f32_16x16x128_f8f6f4 v[106:109], v[180:187], v[212:219], v[106:109], v162, v162 op_sel_hi:[0,0,0]
	v_mfma_scale_f32_16x16x128_f8f6f4 v[94:97], v[172:179], v[220:227], v[94:97], v162, v162 op_sel_hi:[0,0,0]
	v_mfma_scale_f32_16x16x128_f8f6f4 v[90:93], v[180:187], v[220:227], v[90:93], v162, v162 op_sel_hi:[0,0,0]
	s_setprio 0
	s_setprio 1
	v_mfma_scale_f32_16x16x128_f8f6f4 v[134:137], v[2:9], v[196:203], v[134:137], v162, v162 op_sel_hi:[0,0,0]
	v_mfma_scale_f32_16x16x128_f8f6f4 v[130:133], v[188:195], v[196:203], v[130:133], v162, v162 op_sel_hi:[0,0,0]
	v_mfma_scale_f32_16x16x128_f8f6f4 v[118:121], v[2:9], v[204:211], v[118:121], v162, v162 op_sel_hi:[0,0,0]
	v_mfma_scale_f32_16x16x128_f8f6f4 v[114:117], v[188:195], v[204:211], v[114:117], v162, v162 op_sel_hi:[0,0,0]
	v_mfma_scale_f32_16x16x128_f8f6f4 v[102:105], v[2:9], v[212:219], v[102:105], v162, v162 op_sel_hi:[0,0,0]
	v_mfma_scale_f32_16x16x128_f8f6f4 v[98:101], v[188:195], v[212:219], v[98:101], v162, v162 op_sel_hi:[0,0,0]
	v_mfma_scale_f32_16x16x128_f8f6f4 v[86:89], v[2:9], v[220:227], v[86:89], v162, v162 op_sel_hi:[0,0,0]
	v_mfma_scale_f32_16x16x128_f8f6f4 v[82:85], v[188:195], v[220:227], v[82:85], v162, v162 op_sel_hi:[0,0,0]
	s_setprio 0
	s_barrier
	s_add_i32 s48, s65, s25
	v_lshl_add_u64 v[74:75], v[74:75], 0, s[100:101]
	s_mov_b32 m0, s48
	ds_read_b128 v[196:199], v167 offset:49152
	ds_read_b128 v[200:203], v167 offset:50176
	ds_read_b128 v[204:207], v167 offset:51200
	ds_read_b128 v[208:211], v167 offset:52224
	ds_read_b128 v[212:215], v167 offset:53248
	ds_read_b128 v[216:219], v167 offset:54272
	ds_read_b128 v[220:223], v167 offset:55296
	ds_read_b128 v[224:227], v167 offset:56320
	global_load_lds_dwordx4 v[74:75], off
	s_add_i32 m0, s48, 0x2000
	s_add_u32 s46, s46, 0x11000
	v_lshl_add_u64 v[74:75], v[76:77], 0, s[100:101]
	s_addc_u32 s47, s47, 0
	s_add_i32 s48, s66, s25
	global_load_lds_dwordx4 v[74:75], off
	v_lshl_add_u64 v[74:75], s[46:47], 0, v[156:157]
	s_mov_b32 m0, s48
	s_nop 0
	global_load_lds_dwordx4 v[74:75], off
	v_lshl_add_u64 v[74:75], s[46:47], 0, v[150:151]
	s_add_i32 m0, s48, 0x2000
	s_nop 0
	global_load_lds_dwordx4 v[74:75], off
	v_lshl_add_u64 v[74:75], v[78:79], 0, s[16:17]
	s_mov_b32 m0, s56
	s_nop 0
	global_load_lds_dwordx4 v[74:75], off
	v_lshl_add_u64 v[74:75], v[80:81], 0, s[16:17]
	s_mov_b32 m0, s57
	s_nop 0
	global_load_lds_dwordx4 v[74:75], off
	s_waitcnt vmcnt(8)
	s_waitcnt lgkmcnt(0)
	s_barrier
	s_setprio 1
	s_waitcnt lgkmcnt(0)
	v_mfma_scale_f32_16x16x128_f8f6f4 v[70:73], v[172:179], v[196:203], v[70:73], v162, v162 op_sel_hi:[0,0,0]
	v_mfma_scale_f32_16x16x128_f8f6f4 v[66:69], v[180:187], v[196:203], v[66:69], v162, v162 op_sel_hi:[0,0,0]
	v_mfma_scale_f32_16x16x128_f8f6f4 v[54:57], v[172:179], v[204:211], v[54:57], v162, v162 op_sel_hi:[0,0,0]
	v_mfma_scale_f32_16x16x128_f8f6f4 v[50:53], v[180:187], v[204:211], v[50:53], v162, v162 op_sel_hi:[0,0,0]
	v_mfma_scale_f32_16x16x128_f8f6f4 v[38:41], v[172:179], v[212:219], v[38:41], v162, v162 op_sel_hi:[0,0,0]
	v_mfma_scale_f32_16x16x128_f8f6f4 v[34:37], v[180:187], v[212:219], v[34:37], v162, v162 op_sel_hi:[0,0,0]
	v_mfma_scale_f32_16x16x128_f8f6f4 v[18:21], v[172:179], v[220:227], v[18:21], v162, v162 op_sel_hi:[0,0,0]
	v_mfma_scale_f32_16x16x128_f8f6f4 v[22:25], v[180:187], v[220:227], v[22:25], v162, v162 op_sel_hi:[0,0,0]
	s_setprio 0
	s_setprio 1
	v_mfma_scale_f32_16x16x128_f8f6f4 v[62:65], v[2:9], v[196:203], v[62:65], v162, v162 op_sel_hi:[0,0,0]
	v_mfma_scale_f32_16x16x128_f8f6f4 v[58:61], v[188:195], v[196:203], v[58:61], v162, v162 op_sel_hi:[0,0,0]
	v_mfma_scale_f32_16x16x128_f8f6f4 v[46:49], v[2:9], v[204:211], v[46:49], v162, v162 op_sel_hi:[0,0,0]
	v_mfma_scale_f32_16x16x128_f8f6f4 v[42:45], v[188:195], v[204:211], v[42:45], v162, v162 op_sel_hi:[0,0,0]
	v_mfma_scale_f32_16x16x128_f8f6f4 v[30:33], v[2:9], v[212:219], v[30:33], v162, v162 op_sel_hi:[0,0,0]
	v_mfma_scale_f32_16x16x128_f8f6f4 v[26:29], v[188:195], v[212:219], v[26:29], v162, v162 op_sel_hi:[0,0,0]
	v_mfma_scale_f32_16x16x128_f8f6f4 v[10:13], v[2:9], v[220:227], v[10:13], v162, v162 op_sel_hi:[0,0,0]
	v_mfma_scale_f32_16x16x128_f8f6f4 v[14:17], v[188:195], v[220:227], v[14:17], v162, v162 op_sel_hi:[0,0,0]
	s_setprio 0
	s_barrier
	s_add_i32 s18, s18, 2
	s_add_u32 s44, s44, 0x100
	s_addc_u32 s45, s45, 0
	s_add_u32 s1, s1, 0x2000
	s_addc_u32 s13, s13, 0
	s_cmp_gt_u32 s18, 13
	s_cbranch_scc0 .LBB0_1128
	s_and_b64 vcc, exec, s[20:21]
	s_cbranch_vccz .LBB0_1131
	s_barrier
